# all fp8 GEMM K-loops: ds_read bases precomputed per unit, LDS-DMA address adds behind the ds_read groups (no VALU at load-segment heads)
# baseline (speedup 1.0000x reference)
; #define PG8_STAGEA(bufoff, gbase, h) do { if constexpr (GATHER) { PG8_STAGE(bufoff, gbase, vA[h]); } else { PG8_STAGE(bufoff, (gbase) + (h) * hstepA, voffA); } } while (0)
; #define PG8_LDA(dst, b, h) do { _Pragma("unroll") for (int m = 0; m < 4; ++m) _Pragma("unroll") for (int k = 0; k < 2; ++k) dst[m][k] = *(const LAS bf16x8*)(lds + PG8_SA(b, h) + aoff + m * 2048 + k * 1024); } while (0)
; #define PG8_SCHED __builtin_amdgcn_sched_barrier(0)
; template <class Epi, class Sched>
; __device__ __forceinline__ void gemm_phase(const int tid, LAS unsigned char* lds, const char* Abase, const int lda, const int ldb, const int K, const Sched& S, const Epi& E) {
;     ...
; #pragma unroll 1
;         for (int t = 0; t < nt; t += 2) {
;             const bool last = (t == nt - 2);
;             const char* a1 = cA + (size_t)(t + 1) * kstepA;
;             const char* a2 = last ? nA : cA + (size_t)(t + 2) * kstepA; const char* b2 = last ? nB : cB + (size_t)(t + 2) * kstep;
;             const char* a3 = a2 + kstepA; const char* b3 = b2 + kstep;
;             PG8_LDB(B0, 0, 0); PG8_LDB(B1, 0, 1); PG8_SCHED; PG8_LDA(At, 0, 0); PG8_STAGEA(PG8_SA(1, 1), a1, 1);
.LBB0_661:
	s_andn2_b64 vcc, exec, s[46:47]
	s_cbranch_vccnz .LBB0_667
	v_mov_b32_e32 v209, v3
	v_mov_b32_e32 v211, v3
	s_mov_b32 s79, 0
	s_mov_b64 s[2:3], 0x100
	s_waitcnt lgkmcnt(0)
	v_add_u32_e32 v230, 0x10000, v201
	v_add_u32_e32 v231, 0x14000, v201
	v_add_u32_e32 v234, 0x18000, v201
	v_add_u32_e32 v235, 0x1c000, v201
	s_branch .LBB0_665

; #define PG8_STAGEA(bufoff, gbase, h) do { if constexpr (GATHER) { PG8_STAGE(bufoff, gbase, vA[h]); } else { PG8_STAGE(bufoff, (gbase) + (h) * hstepA, voffA); } } while (0)
; #define PG8_LDA(dst, b, h) do { _Pragma("unroll") for (int m = 0; m < 4; ++m) _Pragma("unroll") for (int k = 0; k < 2; ++k) dst[m][k] = *(const LAS bf16x8*)(lds + PG8_SA(b, h) + aoff + m * 2048 + k * 1024); } while (0)
; #define PG8_MM(ai, bj, At, Bt) do { if constexpr (Epi::F8MMA) PG8_MMA8(ai, bj, At, Bt##8); else PG8_MMA(ai, bj, At, Bt); } while (0)
; #define PG8_WAIT_V(n) asm volatile("s_waitcnt vmcnt(" #n ")" ::: "memory")
; #define PG8_WAIT_L(n) asm volatile("s_waitcnt lgkmcnt(" #n ")" ::: "memory")
; #define PG8_BAR __builtin_amdgcn_s_barrier()
; #define PG8_SCHED __builtin_amdgcn_sched_barrier(0)
; template <class Epi, class Sched>
; __device__ __forceinline__ void gemm_phase(const int tid, LAS unsigned char* lds, const char* Abase, const int lda, const int ldb, const int K, const Sched& S, const Epi& E) {
;     ...
;             PG8_WAIT_V(8); PG8_WAIT_L(0); PG8_BAR; PG8_MM(0, 0, At, B0); PG8_MM(0, 1, At, B1); PG8_BAR; PG8_SCHED;
;             PG8_LDA(At, 0, 1); PG8_STAGE(PG8_SB(0, 0), b2, voffB); PG8_STAGE(PG8_SB(0, 1), b2 + hstepB, voffB); PG8_STAGEA(PG8_SA(0, 0), a2, 0);
;             PG8_WAIT_V(8); PG8_WAIT_L(0); PG8_BAR; PG8_MM(1, 0, At, B0); PG8_MM(1, 1, At, B1); PG8_BAR; PG8_SCHED;
.LBB0_664:
	s_add_i32 s79, s79, 2
	s_and_b64 s[56:57], s[60:61], exec
	s_cselect_b32 s57, 0, s2
	s_cselect_b32 s56, 0, s3
	s_add_u32 s64, s38, s57
	s_addc_u32 s65, s39, s56
	s_add_u32 s62, s54, s2
	s_addc_u32 s63, s55, s3
	s_add_u32 s56, s64, 0x80
	s_addc_u32 s57, s65, 0
	s_waitcnt vmcnt(8)
	s_and_b64 s[60:61], s[60:61], exec
	s_waitcnt lgkmcnt(0)
	s_cselect_b32 s60, s52, s62
	s_cselect_b32 s61, s53, s63
	s_add_u32 s62, s60, 0x80
	s_addc_u32 s63, s61, 0
	s_barrier
	s_setprio 1
	s_waitcnt lgkmcnt(0)
	v_mfma_scale_f32_16x16x128_f8f6f4 v[192:195], v[20:27], v[60:67], v[192:195], v219, v216 op_sel_hi:[0,0,0]
	v_mfma_scale_f32_16x16x128_f8f6f4 v[188:191], v[28:35], v[60:67], v[188:191], v219, v216 op_sel_hi:[0,0,0]
	v_mfma_scale_f32_16x16x128_f8f6f4 v[176:179], v[20:27], v[52:59], v[176:179], v219, v216 op_sel_hi:[0,0,0]
	v_mfma_scale_f32_16x16x128_f8f6f4 v[172:175], v[28:35], v[52:59], v[172:175], v219, v216 op_sel_hi:[0,0,0]
	v_mfma_scale_f32_16x16x128_f8f6f4 v[160:163], v[20:27], v[44:51], v[160:163], v219, v216 op_sel_hi:[0,0,0]
	v_mfma_scale_f32_16x16x128_f8f6f4 v[156:159], v[28:35], v[44:51], v[156:159], v219, v216 op_sel_hi:[0,0,0]
	v_mfma_scale_f32_16x16x128_f8f6f4 v[144:147], v[20:27], v[36:43], v[144:147], v219, v216 op_sel_hi:[0,0,0]
	v_mfma_scale_f32_16x16x128_f8f6f4 v[140:143], v[28:35], v[36:43], v[140:143], v219, v216 op_sel_hi:[0,0,0]
	s_setprio 0
	s_setprio 1
	v_mfma_scale_f32_16x16x128_f8f6f4 v[184:187], v[4:11], v[60:67], v[184:187], v219, v216 op_sel_hi:[0,0,0]
	v_mfma_scale_f32_16x16x128_f8f6f4 v[180:183], v[12:19], v[60:67], v[180:183], v219, v216 op_sel_hi:[0,0,0]
	v_mfma_scale_f32_16x16x128_f8f6f4 v[168:171], v[4:11], v[52:59], v[168:171], v219, v216 op_sel_hi:[0,0,0]
	v_mfma_scale_f32_16x16x128_f8f6f4 v[164:167], v[12:19], v[52:59], v[164:167], v219, v216 op_sel_hi:[0,0,0]
	v_mfma_scale_f32_16x16x128_f8f6f4 v[152:155], v[4:11], v[44:51], v[152:155], v219, v216 op_sel_hi:[0,0,0]
	v_mfma_scale_f32_16x16x128_f8f6f4 v[148:151], v[12:19], v[44:51], v[148:151], v219, v216 op_sel_hi:[0,0,0]
	v_mfma_scale_f32_16x16x128_f8f6f4 v[136:139], v[4:11], v[36:43], v[136:139], v219, v216 op_sel_hi:[0,0,0]
	v_mfma_scale_f32_16x16x128_f8f6f4 v[132:135], v[12:19], v[36:43], v[132:135], v219, v216 op_sel_hi:[0,0,0]
	s_setprio 0
	s_barrier
	s_mov_b32 m0, s10
	s_add_u32 s82, s60, 0x8000
	ds_read_b128 v[36:39], v245 offset:16384
	ds_read_b128 v[40:43], v245 offset:17408
	ds_read_b128 v[44:47], v245 offset:18432
	ds_read_b128 v[48:51], v245 offset:19456
	ds_read_b128 v[52:55], v245 offset:20480
	ds_read_b128 v[56:59], v245 offset:21504
	ds_read_b128 v[60:63], v245 offset:22528
	ds_read_b128 v[64:67], v245 offset:23552
	v_lshl_add_u64 v[228:229], s[60:61], 0, v[198:199]
	global_load_lds_dwordx4 v[228:229], off
	v_lshl_add_u64 v[228:229], s[60:61], 0, v[196:197]
	s_mov_b32 m0, s11
	s_addc_u32 s83, s61, 0
	global_load_lds_dwordx4 v[228:229], off
	v_lshl_add_u64 v[228:229], s[82:83], 0, v[198:199]
	s_mov_b32 m0, s22
	s_nop 0
	global_load_lds_dwordx4 v[228:229], off
	v_lshl_add_u64 v[228:229], s[82:83], 0, v[196:197]
	s_mov_b32 m0, s25
	s_nop 0
	global_load_lds_dwordx4 v[228:229], off
	s_mov_b32 m0, s9
	s_nop 0
	global_load_lds_dwordx4 v200, s[64:65]
	s_mov_b32 m0, s28
	s_nop 0
	global_load_lds_dwordx4 v202, s[64:65]
	s_waitcnt vmcnt(8)
	s_waitcnt lgkmcnt(0)
	s_barrier
	s_setprio 1
	s_waitcnt lgkmcnt(0)
	v_mfma_scale_f32_16x16x128_f8f6f4 v[128:131], v[20:27], v[36:43], v[128:131], v219, v216 op_sel_hi:[0,0,0]
	v_mfma_scale_f32_16x16x128_f8f6f4 v[124:127], v[28:35], v[36:43], v[124:127], v219, v216 op_sel_hi:[0,0,0]
	v_mfma_scale_f32_16x16x128_f8f6f4 v[112:115], v[20:27], v[44:51], v[112:115], v219, v216 op_sel_hi:[0,0,0]
	v_mfma_scale_f32_16x16x128_f8f6f4 v[108:111], v[28:35], v[44:51], v[108:111], v219, v216 op_sel_hi:[0,0,0]
	v_mfma_scale_f32_16x16x128_f8f6f4 v[96:99], v[20:27], v[52:59], v[96:99], v219, v216 op_sel_hi:[0,0,0]
	v_mfma_scale_f32_16x16x128_f8f6f4 v[92:95], v[28:35], v[52:59], v[92:95], v219, v216 op_sel_hi:[0,0,0]
	v_mfma_scale_f32_16x16x128_f8f6f4 v[80:83], v[20:27], v[60:67], v[80:83], v219, v216 op_sel_hi:[0,0,0]
	v_mfma_scale_f32_16x16x128_f8f6f4 v[76:79], v[28:35], v[60:67], v[76:79], v219, v216 op_sel_hi:[0,0,0]
	s_setprio 0
	s_setprio 1
	v_mfma_scale_f32_16x16x128_f8f6f4 v[120:123], v[4:11], v[36:43], v[120:123], v219, v216 op_sel_hi:[0,0,0]
	v_mfma_scale_f32_16x16x128_f8f6f4 v[116:119], v[12:19], v[36:43], v[116:119], v219, v216 op_sel_hi:[0,0,0]
	v_mfma_scale_f32_16x16x128_f8f6f4 v[104:107], v[4:11], v[44:51], v[104:107], v219, v216 op_sel_hi:[0,0,0]
	v_mfma_scale_f32_16x16x128_f8f6f4 v[100:103], v[12:19], v[44:51], v[100:103], v219, v216 op_sel_hi:[0,0,0]
	v_mfma_scale_f32_16x16x128_f8f6f4 v[88:91], v[4:11], v[52:59], v[88:91], v219, v216 op_sel_hi:[0,0,0]
	v_mfma_scale_f32_16x16x128_f8f6f4 v[84:87], v[12:19], v[52:59], v[84:87], v219, v216 op_sel_hi:[0,0,0]
	v_mfma_scale_f32_16x16x128_f8f6f4 v[72:75], v[4:11], v[60:67], v[72:75], v219, v216 op_sel_hi:[0,0,0]
	v_mfma_scale_f32_16x16x128_f8f6f4 v[68:71], v[12:19], v[60:67], v[68:71], v219, v216 op_sel_hi:[0,0,0]
	s_setprio 0
	s_barrier
; #define PG8_STAGEA(bufoff, gbase, h) do { if constexpr (GATHER) { PG8_STAGE(bufoff, gbase, vA[h]); } else { PG8_STAGE(bufoff, (gbase) + (h) * hstepA, voffA); } } while (0)
; #define PG8_LDA(dst, b, h) do { _Pragma("unroll") for (int m = 0; m < 4; ++m) _Pragma("unroll") for (int k = 0; k < 2; ++k) dst[m][k] = *(const LAS bf16x8*)(lds + PG8_SA(b, h) + aoff + m * 2048 + k * 1024); } while (0)
; #define PG8_MM(ai, bj, At, Bt) do { if constexpr (Epi::F8MMA) PG8_MMA8(ai, bj, At, Bt##8); else PG8_MMA(ai, bj, At, Bt); } while (0)
; #define PG8_WAIT_V(n) asm volatile("s_waitcnt vmcnt(" #n ")" ::: "memory")
; #define PG8_WAIT_L(n) asm volatile("s_waitcnt lgkmcnt(" #n ")" ::: "memory")
; #define PG8_BAR __builtin_amdgcn_s_barrier()
; #define PG8_SCHED __builtin_amdgcn_sched_barrier(0)
; template <class Epi, class Sched>
; __device__ __forceinline__ void gemm_phase(const int tid, LAS unsigned char* lds, const char* Abase, const int lda, const int ldb, const int K, const Sched& S, const Epi& E) {
;     ...
;             PG8_LDB(B0, 0, 0); PG8_LDB(B1, 0, 1); PG8_SCHED; PG8_LDA(At, 0, 0); PG8_STAGEA(PG8_SA(1, 1), a1, 1);
;     ...
;             PG8_LDA(At, 0, 1); PG8_STAGE(PG8_SB(0, 0), b2, voffB); PG8_STAGE(PG8_SB(0, 1), b2 + hstepB, voffB); PG8_STAGEA(PG8_SA(0, 0), a2, 0);
;             PG8_WAIT_V(8); PG8_WAIT_L(0); PG8_BAR; PG8_MM(1, 0, At, B0); PG8_MM(1, 1, At, B1); PG8_BAR; PG8_SCHED;
;             PG8_LDB(B0, 1, 0); PG8_LDB(B1, 1, 1); PG8_SCHED; PG8_LDA(At, 1, 0); PG8_STAGEA(PG8_SA(0, 1), a2, 1);
;             PG8_WAIT_V(8); PG8_WAIT_L(0); PG8_BAR; PG8_MM(0, 0, At, B0); PG8_MM(0, 1, At, B1); PG8_BAR; PG8_SCHED;
;             PG8_LDA(At, 1, 1); PG8_STAGE(PG8_SB(1, 0), b3, voffB); PG8_STAGE(PG8_SB(1, 1), b3 + hstepB, voffB); PG8_STAGEA(PG8_SA(1, 0), a3, 0);
;             PG8_WAIT_V(8); PG8_WAIT_L(0); PG8_BAR; PG8_MM(1, 0, At, B0); PG8_MM(1, 1, At, B1); PG8_BAR; PG8_SCHED;
.Lmid_ao:
	s_add_i32 s82, 0, 0x18000
	s_add_i32 s83, 0, 0x1c000
	ds_read_b128 v[4:7], v234
	ds_read_b128 v[8:11], v234 offset:1024
	ds_read_b128 v[12:15], v234 offset:2048
	ds_read_b128 v[16:19], v234 offset:3072
	ds_read_b128 v[20:23], v235
	ds_read_b128 v[24:27], v235 offset:1024
	ds_read_b128 v[28:31], v235 offset:2048
	ds_read_b128 v[32:35], v235 offset:3072
	s_mov_b32 m0, s29
	ds_read_b128 v[36:39], v245 offset:32768
	ds_read_b128 v[40:43], v245 offset:33792
	ds_read_b128 v[44:47], v245 offset:34816
	ds_read_b128 v[48:51], v245 offset:35840
	ds_read_b128 v[52:55], v245 offset:36864
	ds_read_b128 v[56:59], v245 offset:37888
	ds_read_b128 v[60:63], v245 offset:38912
	ds_read_b128 v[64:67], v245 offset:39936
	v_lshl_add_u64 v[214:215], s[64:65], 0, v[214:215]
	global_load_lds_dwordx4 v[214:215], off
	v_lshl_add_u64 v[212:213], s[64:65], 0, v[212:213]
	s_mov_b32 m0, s66
	s_nop 0
	global_load_lds_dwordx4 v[212:213], off
	s_waitcnt vmcnt(8)
	s_waitcnt lgkmcnt(0)
	s_barrier
	s_setprio 1
	s_waitcnt lgkmcnt(0)
	v_mfma_scale_f32_16x16x128_f8f6f4 v[192:195], v[4:11], v[36:43], v[192:195], v219, v216 op_sel_hi:[0,0,0]
	v_mfma_scale_f32_16x16x128_f8f6f4 v[188:191], v[12:19], v[36:43], v[188:191], v219, v216 op_sel_hi:[0,0,0]
	v_mfma_scale_f32_16x16x128_f8f6f4 v[176:179], v[4:11], v[44:51], v[176:179], v219, v216 op_sel_hi:[0,0,0]
	v_mfma_scale_f32_16x16x128_f8f6f4 v[172:175], v[12:19], v[44:51], v[172:175], v219, v216 op_sel_hi:[0,0,0]
	v_mfma_scale_f32_16x16x128_f8f6f4 v[160:163], v[4:11], v[52:59], v[160:163], v219, v216 op_sel_hi:[0,0,0]
	v_mfma_scale_f32_16x16x128_f8f6f4 v[156:159], v[12:19], v[52:59], v[156:159], v219, v216 op_sel_hi:[0,0,0]
	v_mfma_scale_f32_16x16x128_f8f6f4 v[144:147], v[4:11], v[60:67], v[144:147], v219, v216 op_sel_hi:[0,0,0]
	v_mfma_scale_f32_16x16x128_f8f6f4 v[140:143], v[12:19], v[60:67], v[140:143], v219, v216 op_sel_hi:[0,0,0]
	s_setprio 0
	s_setprio 1
	v_mfma_scale_f32_16x16x128_f8f6f4 v[184:187], v[20:27], v[36:43], v[184:187], v219, v216 op_sel_hi:[0,0,0]
	v_mfma_scale_f32_16x16x128_f8f6f4 v[180:183], v[28:35], v[36:43], v[180:183], v219, v216 op_sel_hi:[0,0,0]
	v_mfma_scale_f32_16x16x128_f8f6f4 v[168:171], v[20:27], v[44:51], v[168:171], v219, v216 op_sel_hi:[0,0,0]
	v_mfma_scale_f32_16x16x128_f8f6f4 v[164:167], v[28:35], v[44:51], v[164:167], v219, v216 op_sel_hi:[0,0,0]
	v_mfma_scale_f32_16x16x128_f8f6f4 v[152:155], v[20:27], v[52:59], v[152:155], v219, v216 op_sel_hi:[0,0,0]
	v_mfma_scale_f32_16x16x128_f8f6f4 v[148:151], v[28:35], v[52:59], v[148:151], v219, v216 op_sel_hi:[0,0,0]
	v_mfma_scale_f32_16x16x128_f8f6f4 v[136:139], v[20:27], v[60:67], v[136:139], v219, v216 op_sel_hi:[0,0,0]
	v_mfma_scale_f32_16x16x128_f8f6f4 v[132:135], v[28:35], v[60:67], v[132:135], v219, v216 op_sel_hi:[0,0,0]
	s_setprio 0
	s_barrier
	s_add_i32 s64, s82, s8
	s_mov_b32 m0, s64
	ds_read_b128 v[36:39], v245 offset:49152
	ds_read_b128 v[40:43], v245 offset:50176
	ds_read_b128 v[44:47], v245 offset:51200
	ds_read_b128 v[48:51], v245 offset:52224
	ds_read_b128 v[52:55], v245 offset:53248
	ds_read_b128 v[56:59], v245 offset:54272
	ds_read_b128 v[60:63], v245 offset:55296
	ds_read_b128 v[64:67], v245 offset:56320
	v_lshl_add_u64 v[212:213], s[62:63], 0, v[198:199]
	global_load_lds_dwordx4 v[212:213], off
	s_add_i32 m0, s64, 0x2000
	s_add_u32 s60, s60, 0x8080
	v_lshl_add_u64 v[212:213], s[62:63], 0, v[196:197]
	s_addc_u32 s61, s61, 0
	s_add_i32 s62, s83, s8
	global_load_lds_dwordx4 v[212:213], off
	v_lshl_add_u64 v[212:213], s[60:61], 0, v[198:199]
	s_mov_b32 m0, s62
	s_nop 0
	global_load_lds_dwordx4 v[212:213], off
	v_lshl_add_u64 v[212:213], s[60:61], 0, v[196:197]
	s_add_i32 m0, s62, 0x2000
	s_nop 0
	global_load_lds_dwordx4 v[212:213], off
	s_mov_b32 m0, s67
	s_nop 0
	global_load_lds_dwordx4 v200, s[56:57]
	s_mov_b32 m0, s68
	s_nop 0
	global_load_lds_dwordx4 v202, s[56:57]
	s_waitcnt vmcnt(8)
	s_waitcnt lgkmcnt(0)
	s_barrier
	s_setprio 1
	s_waitcnt lgkmcnt(0)
	v_mfma_scale_f32_16x16x128_f8f6f4 v[128:131], v[4:11], v[36:43], v[128:131], v219, v216 op_sel_hi:[0,0,0]
	v_mfma_scale_f32_16x16x128_f8f6f4 v[124:127], v[12:19], v[36:43], v[124:127], v219, v216 op_sel_hi:[0,0,0]
	v_mfma_scale_f32_16x16x128_f8f6f4 v[112:115], v[4:11], v[44:51], v[112:115], v219, v216 op_sel_hi:[0,0,0]
	v_mfma_scale_f32_16x16x128_f8f6f4 v[108:111], v[12:19], v[44:51], v[108:111], v219, v216 op_sel_hi:[0,0,0]
	v_mfma_scale_f32_16x16x128_f8f6f4 v[96:99], v[4:11], v[52:59], v[96:99], v219, v216 op_sel_hi:[0,0,0]
	v_mfma_scale_f32_16x16x128_f8f6f4 v[92:95], v[12:19], v[52:59], v[92:95], v219, v216 op_sel_hi:[0,0,0]
	v_mfma_scale_f32_16x16x128_f8f6f4 v[80:83], v[4:11], v[60:67], v[80:83], v219, v216 op_sel_hi:[0,0,0]
	v_mfma_scale_f32_16x16x128_f8f6f4 v[76:79], v[12:19], v[60:67], v[76:79], v219, v216 op_sel_hi:[0,0,0]
	s_setprio 0
	s_setprio 1
	v_mfma_scale_f32_16x16x128_f8f6f4 v[120:123], v[20:27], v[36:43], v[120:123], v219, v216 op_sel_hi:[0,0,0]
	v_mfma_scale_f32_16x16x128_f8f6f4 v[116:119], v[28:35], v[36:43], v[116:119], v219, v216 op_sel_hi:[0,0,0]
	v_mfma_scale_f32_16x16x128_f8f6f4 v[104:107], v[20:27], v[44:51], v[104:107], v219, v216 op_sel_hi:[0,0,0]
	v_mfma_scale_f32_16x16x128_f8f6f4 v[100:103], v[28:35], v[44:51], v[100:103], v219, v216 op_sel_hi:[0,0,0]
	v_mfma_scale_f32_16x16x128_f8f6f4 v[88:91], v[20:27], v[52:59], v[88:91], v219, v216 op_sel_hi:[0,0,0]
	v_mfma_scale_f32_16x16x128_f8f6f4 v[84:87], v[28:35], v[52:59], v[84:87], v219, v216 op_sel_hi:[0,0,0]
	v_mfma_scale_f32_16x16x128_f8f6f4 v[72:75], v[20:27], v[60:67], v[72:75], v219, v216 op_sel_hi:[0,0,0]
	v_mfma_scale_f32_16x16x128_f8f6f4 v[68:71], v[28:35], v[60:67], v[68:71], v219, v216 op_sel_hi:[0,0,0]
	s_setprio 0
	s_barrier
	s_add_u32 s2, s2, 0x100
	s_addc_u32 s3, s3, 0
	s_cmp_ge_i32 s79, s5
	s_cbranch_scc1 .LBB0_668
.LBB0_665:
	ds_read_b128 v[20:23], v230
	ds_read_b128 v[24:27], v230 offset:1024
	ds_read_b128 v[28:31], v230 offset:2048
	ds_read_b128 v[32:35], v230 offset:3072
	ds_read_b128 v[4:7], v231
	ds_read_b128 v[8:11], v231 offset:1024
	ds_read_b128 v[12:15], v231 offset:2048
	ds_read_b128 v[16:19], v231 offset:3072
	s_cmp_eq_u32 s70, s79
	s_cselect_b64 s[60:61], -1, 0
	s_add_u32 s56, s38, s2
	s_addc_u32 s57, s39, s3
	s_add_u32 s56, s56, 0xffffff80
	s_addc_u32 s57, s57, -1
	s_add_i32 m0, s9, 0xc000
	s_add_i32 s62, s9, 0xe000
	s_cmp_lg_u32 s70, s79
	ds_read_b128 v[60:63], v245
	ds_read_b128 v[64:67], v245 offset:1024
	ds_read_b128 v[52:55], v245 offset:2048
	ds_read_b128 v[56:59], v245 offset:3072
	ds_read_b128 v[44:47], v245 offset:4096
	ds_read_b128 v[48:51], v245 offset:5120
	ds_read_b128 v[36:39], v245 offset:6144
	ds_read_b128 v[40:43], v245 offset:7168
	global_load_lds_dwordx4 v2, s[56:57]
	s_mov_b32 m0, s62
	s_nop 0
	global_load_lds_dwordx4 v204, s[56:57]
	s_cbranch_scc0 .LBB0_663
	v_mov_b32_e32 v205, v3
	v_mov_b64_e32 v[212:213], v[204:205]
	v_mov_b64_e32 v[214:215], v[2:3]
	s_cmp_eq_u32 s79, 0
	s_cbranch_scc1 .Lpeel_ao
	s_branch .LBB0_664

; #define PG8_STAGEA(bufoff, gbase, h) do { if constexpr (GATHER) { PG8_STAGE(bufoff, gbase, vA[h]); } else { PG8_STAGE(bufoff, (gbase) + (h) * hstepA, voffA); } } while (0)
; #define PG8_LDA(dst, b, h) do { _Pragma("unroll") for (int m = 0; m < 4; ++m) _Pragma("unroll") for (int k = 0; k < 2; ++k) dst[m][k] = *(const LAS bf16x8*)(lds + PG8_SA(b, h) + aoff + m * 2048 + k * 1024); } while (0)
; #define PG8_SCHED __builtin_amdgcn_sched_barrier(0)
; template <class Epi, class Sched>
; __device__ __forceinline__ void gemm_phase(const int tid, LAS unsigned char* lds, const char* Abase, const int lda, const int ldb, const int K, const Sched& S, const Epi& E) {
;     ...
; #pragma unroll 1
;         for (int t = 0; t < nt; t += 2) {
;             const bool last = (t == nt - 2);
;             const char* a1 = cA + (size_t)(t + 1) * kstepA;
;             const char* a2 = last ? nA : cA + (size_t)(t + 2) * kstepA; const char* b2 = last ? nB : cB + (size_t)(t + 2) * kstep;
;             const char* a3 = a2 + kstepA; const char* b3 = b2 + kstep;
;             PG8_LDB(B0, 0, 0); PG8_LDB(B1, 0, 1); PG8_SCHED; PG8_LDA(At, 0, 0); PG8_STAGEA(PG8_SA(1, 1), a1, 1);
.LBB0_768:
	s_andn2_b64 vcc, exec, s[48:49]
	s_cbranch_vccnz .LBB0_774
	v_mov_b32_e32 v209, v3
	v_mov_b32_e32 v211, v3
	s_mov_b32 s83, 0
	s_mov_b64 s[2:3], 0x100
	s_waitcnt lgkmcnt(0)
	v_add_u32_e32 v230, 0x10000, v201
	v_add_u32_e32 v231, 0x14000, v201
	v_add_u32_e32 v234, 0x18000, v201
	v_add_u32_e32 v235, 0x1c000, v201
	s_branch .LBB0_772

; #define PG8_STAGEA(bufoff, gbase, h) do { if constexpr (GATHER) { PG8_STAGE(bufoff, gbase, vA[h]); } else { PG8_STAGE(bufoff, (gbase) + (h) * hstepA, voffA); } } while (0)
; #define PG8_LDA(dst, b, h) do { _Pragma("unroll") for (int m = 0; m < 4; ++m) _Pragma("unroll") for (int k = 0; k < 2; ++k) dst[m][k] = *(const LAS bf16x8*)(lds + PG8_SA(b, h) + aoff + m * 2048 + k * 1024); } while (0)
; #define PG8_MM(ai, bj, At, Bt) do { if constexpr (Epi::F8MMA) PG8_MMA8(ai, bj, At, Bt##8); else PG8_MMA(ai, bj, At, Bt); } while (0)
; #define PG8_WAIT_V(n) asm volatile("s_waitcnt vmcnt(" #n ")" ::: "memory")
; #define PG8_WAIT_L(n) asm volatile("s_waitcnt lgkmcnt(" #n ")" ::: "memory")
; #define PG8_BAR __builtin_amdgcn_s_barrier()
; #define PG8_SCHED __builtin_amdgcn_sched_barrier(0)
; template <class Epi, class Sched>
; __device__ __forceinline__ void gemm_phase(const int tid, LAS unsigned char* lds, const char* Abase, const int lda, const int ldb, const int K, const Sched& S, const Epi& E) {
;     ...
;             PG8_WAIT_V(8); PG8_WAIT_L(0); PG8_BAR; PG8_MM(0, 0, At, B0); PG8_MM(0, 1, At, B1); PG8_BAR; PG8_SCHED;
;             PG8_LDA(At, 0, 1); PG8_STAGE(PG8_SB(0, 0), b2, voffB); PG8_STAGE(PG8_SB(0, 1), b2 + hstepB, voffB); PG8_STAGEA(PG8_SA(0, 0), a2, 0);
;             PG8_WAIT_V(8); PG8_WAIT_L(0); PG8_BAR; PG8_MM(1, 0, At, B0); PG8_MM(1, 1, At, B1); PG8_BAR; PG8_SCHED;
.LBB0_771:
	s_add_i32 s83, s83, 2
	s_and_b64 s[60:61], s[62:63], exec
	s_cselect_b32 s61, 0, s2
	s_cselect_b32 s60, 0, s3
	s_add_u32 s66, s42, s61
	s_addc_u32 s67, s43, s60
	s_add_u32 s64, s56, s2
	s_addc_u32 s65, s57, s3
	s_add_u32 s60, s66, 0x80
	s_addc_u32 s61, s67, 0
	s_waitcnt vmcnt(8)
	s_and_b64 s[62:63], s[62:63], exec
	s_waitcnt lgkmcnt(0)
	s_cselect_b32 s62, s54, s64
	s_cselect_b32 s63, s55, s65
	s_add_u32 s64, s62, 0x80
	s_addc_u32 s65, s63, 0
	s_barrier
	s_setprio 1
	s_waitcnt lgkmcnt(0)
	v_mfma_scale_f32_16x16x128_f8f6f4 v[192:195], v[20:27], v[60:67], v[192:195], v220, v216 op_sel_hi:[0,0,0]
	v_mfma_scale_f32_16x16x128_f8f6f4 v[188:191], v[28:35], v[60:67], v[188:191], v220, v216 op_sel_hi:[0,0,0]
	v_mfma_scale_f32_16x16x128_f8f6f4 v[176:179], v[20:27], v[52:59], v[176:179], v220, v216 op_sel_hi:[0,0,0]
	v_mfma_scale_f32_16x16x128_f8f6f4 v[172:175], v[28:35], v[52:59], v[172:175], v220, v216 op_sel_hi:[0,0,0]
	v_mfma_scale_f32_16x16x128_f8f6f4 v[160:163], v[20:27], v[44:51], v[160:163], v220, v216 op_sel_hi:[0,0,0]
	v_mfma_scale_f32_16x16x128_f8f6f4 v[156:159], v[28:35], v[44:51], v[156:159], v220, v216 op_sel_hi:[0,0,0]
	v_mfma_scale_f32_16x16x128_f8f6f4 v[144:147], v[20:27], v[36:43], v[144:147], v220, v216 op_sel_hi:[0,0,0]
	v_mfma_scale_f32_16x16x128_f8f6f4 v[140:143], v[28:35], v[36:43], v[140:143], v220, v216 op_sel_hi:[0,0,0]
	s_setprio 0
	s_setprio 1
	v_mfma_scale_f32_16x16x128_f8f6f4 v[184:187], v[4:11], v[60:67], v[184:187], v220, v216 op_sel_hi:[0,0,0]
	v_mfma_scale_f32_16x16x128_f8f6f4 v[180:183], v[12:19], v[60:67], v[180:183], v220, v216 op_sel_hi:[0,0,0]
	v_mfma_scale_f32_16x16x128_f8f6f4 v[168:171], v[4:11], v[52:59], v[168:171], v220, v216 op_sel_hi:[0,0,0]
	v_mfma_scale_f32_16x16x128_f8f6f4 v[164:167], v[12:19], v[52:59], v[164:167], v220, v216 op_sel_hi:[0,0,0]
	v_mfma_scale_f32_16x16x128_f8f6f4 v[152:155], v[4:11], v[44:51], v[152:155], v220, v216 op_sel_hi:[0,0,0]
	v_mfma_scale_f32_16x16x128_f8f6f4 v[148:151], v[12:19], v[44:51], v[148:151], v220, v216 op_sel_hi:[0,0,0]
	v_mfma_scale_f32_16x16x128_f8f6f4 v[136:139], v[4:11], v[36:43], v[136:139], v220, v216 op_sel_hi:[0,0,0]
	v_mfma_scale_f32_16x16x128_f8f6f4 v[132:135], v[12:19], v[36:43], v[132:135], v220, v216 op_sel_hi:[0,0,0]
	s_setprio 0
	s_barrier
	s_mov_b32 m0, s10
	s_add_u32 s86, s62, 0x8000
	ds_read_b128 v[36:39], v243 offset:16384
	ds_read_b128 v[40:43], v243 offset:17408
	ds_read_b128 v[44:47], v243 offset:18432
	ds_read_b128 v[48:51], v243 offset:19456
	ds_read_b128 v[52:55], v243 offset:20480
	ds_read_b128 v[56:59], v243 offset:21504
	ds_read_b128 v[60:63], v243 offset:22528
	ds_read_b128 v[64:67], v243 offset:23552
	v_lshl_add_u64 v[228:229], s[62:63], 0, v[198:199]
	global_load_lds_dwordx4 v[228:229], off
	v_lshl_add_u64 v[228:229], s[62:63], 0, v[196:197]
	s_mov_b32 m0, s11
	s_addc_u32 s87, s63, 0
	global_load_lds_dwordx4 v[228:229], off
	v_lshl_add_u64 v[228:229], s[86:87], 0, v[198:199]
	s_mov_b32 m0, s22
	s_nop 0
	global_load_lds_dwordx4 v[228:229], off
	v_lshl_add_u64 v[228:229], s[86:87], 0, v[196:197]
	s_mov_b32 m0, s25
	s_nop 0
	global_load_lds_dwordx4 v[228:229], off
	s_mov_b32 m0, s9
	s_nop 0
	global_load_lds_dwordx4 v200, s[66:67]
	s_mov_b32 m0, s28
	s_nop 0
	global_load_lds_dwordx4 v202, s[66:67]
	s_waitcnt vmcnt(8)
	s_waitcnt lgkmcnt(0)
	s_barrier
	s_setprio 1
	s_waitcnt lgkmcnt(0)
	v_mfma_scale_f32_16x16x128_f8f6f4 v[128:131], v[20:27], v[36:43], v[128:131], v220, v216 op_sel_hi:[0,0,0]
	v_mfma_scale_f32_16x16x128_f8f6f4 v[124:127], v[28:35], v[36:43], v[124:127], v220, v216 op_sel_hi:[0,0,0]
	v_mfma_scale_f32_16x16x128_f8f6f4 v[112:115], v[20:27], v[44:51], v[112:115], v220, v216 op_sel_hi:[0,0,0]
	v_mfma_scale_f32_16x16x128_f8f6f4 v[108:111], v[28:35], v[44:51], v[108:111], v220, v216 op_sel_hi:[0,0,0]
	v_mfma_scale_f32_16x16x128_f8f6f4 v[96:99], v[20:27], v[52:59], v[96:99], v220, v216 op_sel_hi:[0,0,0]
	v_mfma_scale_f32_16x16x128_f8f6f4 v[92:95], v[28:35], v[52:59], v[92:95], v220, v216 op_sel_hi:[0,0,0]
	v_mfma_scale_f32_16x16x128_f8f6f4 v[80:83], v[20:27], v[60:67], v[80:83], v220, v216 op_sel_hi:[0,0,0]
	v_mfma_scale_f32_16x16x128_f8f6f4 v[76:79], v[28:35], v[60:67], v[76:79], v220, v216 op_sel_hi:[0,0,0]
	s_setprio 0
	s_setprio 1
	v_mfma_scale_f32_16x16x128_f8f6f4 v[120:123], v[4:11], v[36:43], v[120:123], v220, v216 op_sel_hi:[0,0,0]
	v_mfma_scale_f32_16x16x128_f8f6f4 v[116:119], v[12:19], v[36:43], v[116:119], v220, v216 op_sel_hi:[0,0,0]
	v_mfma_scale_f32_16x16x128_f8f6f4 v[104:107], v[4:11], v[44:51], v[104:107], v220, v216 op_sel_hi:[0,0,0]
	v_mfma_scale_f32_16x16x128_f8f6f4 v[100:103], v[12:19], v[44:51], v[100:103], v220, v216 op_sel_hi:[0,0,0]
	v_mfma_scale_f32_16x16x128_f8f6f4 v[88:91], v[4:11], v[52:59], v[88:91], v220, v216 op_sel_hi:[0,0,0]
	v_mfma_scale_f32_16x16x128_f8f6f4 v[84:87], v[12:19], v[52:59], v[84:87], v220, v216 op_sel_hi:[0,0,0]
	v_mfma_scale_f32_16x16x128_f8f6f4 v[72:75], v[4:11], v[60:67], v[72:75], v220, v216 op_sel_hi:[0,0,0]
	v_mfma_scale_f32_16x16x128_f8f6f4 v[68:71], v[12:19], v[60:67], v[68:71], v220, v216 op_sel_hi:[0,0,0]
	s_setprio 0
	s_barrier
; #define PG8_STAGEA(bufoff, gbase, h) do { if constexpr (GATHER) { PG8_STAGE(bufoff, gbase, vA[h]); } else { PG8_STAGE(bufoff, (gbase) + (h) * hstepA, voffA); } } while (0)
; #define PG8_LDA(dst, b, h) do { _Pragma("unroll") for (int m = 0; m < 4; ++m) _Pragma("unroll") for (int k = 0; k < 2; ++k) dst[m][k] = *(const LAS bf16x8*)(lds + PG8_SA(b, h) + aoff + m * 2048 + k * 1024); } while (0)
; #define PG8_MM(ai, bj, At, Bt) do { if constexpr (Epi::F8MMA) PG8_MMA8(ai, bj, At, Bt##8); else PG8_MMA(ai, bj, At, Bt); } while (0)
; #define PG8_WAIT_V(n) asm volatile("s_waitcnt vmcnt(" #n ")" ::: "memory")
; #define PG8_WAIT_L(n) asm volatile("s_waitcnt lgkmcnt(" #n ")" ::: "memory")
; #define PG8_BAR __builtin_amdgcn_s_barrier()
; #define PG8_SCHED __builtin_amdgcn_sched_barrier(0)
; template <class Epi, class Sched>
; __device__ __forceinline__ void gemm_phase(const int tid, LAS unsigned char* lds, const char* Abase, const int lda, const int ldb, const int K, const Sched& S, const Epi& E) {
;     ...
;             PG8_LDB(B0, 0, 0); PG8_LDB(B1, 0, 1); PG8_SCHED; PG8_LDA(At, 0, 0); PG8_STAGEA(PG8_SA(1, 1), a1, 1);
;     ...
;             PG8_LDA(At, 0, 1); PG8_STAGE(PG8_SB(0, 0), b2, voffB); PG8_STAGE(PG8_SB(0, 1), b2 + hstepB, voffB); PG8_STAGEA(PG8_SA(0, 0), a2, 0);
;             PG8_WAIT_V(8); PG8_WAIT_L(0); PG8_BAR; PG8_MM(1, 0, At, B0); PG8_MM(1, 1, At, B1); PG8_BAR; PG8_SCHED;
;             PG8_LDB(B0, 1, 0); PG8_LDB(B1, 1, 1); PG8_SCHED; PG8_LDA(At, 1, 0); PG8_STAGEA(PG8_SA(0, 1), a2, 1);
;             PG8_WAIT_V(8); PG8_WAIT_L(0); PG8_BAR; PG8_MM(0, 0, At, B0); PG8_MM(0, 1, At, B1); PG8_BAR; PG8_SCHED;
;             PG8_LDA(At, 1, 1); PG8_STAGE(PG8_SB(1, 0), b3, voffB); PG8_STAGE(PG8_SB(1, 1), b3 + hstepB, voffB); PG8_STAGEA(PG8_SA(1, 0), a3, 0);
;             PG8_WAIT_V(8); PG8_WAIT_L(0); PG8_BAR; PG8_MM(1, 0, At, B0); PG8_MM(1, 1, At, B1); PG8_BAR; PG8_SCHED;
.Lmid_pi:
	s_add_i32 s86, 0, 0x18000
	s_add_i32 s87, 0, 0x1c000
	ds_read_b128 v[4:7], v234
	ds_read_b128 v[8:11], v234 offset:1024
	ds_read_b128 v[12:15], v234 offset:2048
	ds_read_b128 v[16:19], v234 offset:3072
	ds_read_b128 v[20:23], v235
	ds_read_b128 v[24:27], v235 offset:1024
	ds_read_b128 v[28:31], v235 offset:2048
	ds_read_b128 v[32:35], v235 offset:3072
	s_mov_b32 m0, s29
	ds_read_b128 v[36:39], v243 offset:32768
	ds_read_b128 v[40:43], v243 offset:33792
	ds_read_b128 v[44:47], v243 offset:34816
	ds_read_b128 v[48:51], v243 offset:35840
	ds_read_b128 v[52:55], v243 offset:36864
	ds_read_b128 v[56:59], v243 offset:37888
	ds_read_b128 v[60:63], v243 offset:38912
	ds_read_b128 v[64:67], v243 offset:39936
	v_lshl_add_u64 v[214:215], s[66:67], 0, v[214:215]
	global_load_lds_dwordx4 v[214:215], off
	v_lshl_add_u64 v[212:213], s[66:67], 0, v[212:213]
	s_mov_b32 m0, s68
	s_nop 0
	global_load_lds_dwordx4 v[212:213], off
	s_waitcnt vmcnt(8)
	s_waitcnt lgkmcnt(0)
	s_barrier
	s_setprio 1
	s_waitcnt lgkmcnt(0)
	v_mfma_scale_f32_16x16x128_f8f6f4 v[192:195], v[4:11], v[36:43], v[192:195], v220, v216 op_sel_hi:[0,0,0]
	v_mfma_scale_f32_16x16x128_f8f6f4 v[188:191], v[12:19], v[36:43], v[188:191], v220, v216 op_sel_hi:[0,0,0]
	v_mfma_scale_f32_16x16x128_f8f6f4 v[176:179], v[4:11], v[44:51], v[176:179], v220, v216 op_sel_hi:[0,0,0]
	v_mfma_scale_f32_16x16x128_f8f6f4 v[172:175], v[12:19], v[44:51], v[172:175], v220, v216 op_sel_hi:[0,0,0]
	v_mfma_scale_f32_16x16x128_f8f6f4 v[160:163], v[4:11], v[52:59], v[160:163], v220, v216 op_sel_hi:[0,0,0]
	v_mfma_scale_f32_16x16x128_f8f6f4 v[156:159], v[12:19], v[52:59], v[156:159], v220, v216 op_sel_hi:[0,0,0]
	v_mfma_scale_f32_16x16x128_f8f6f4 v[144:147], v[4:11], v[60:67], v[144:147], v220, v216 op_sel_hi:[0,0,0]
	v_mfma_scale_f32_16x16x128_f8f6f4 v[140:143], v[12:19], v[60:67], v[140:143], v220, v216 op_sel_hi:[0,0,0]
	s_setprio 0
	s_setprio 1
	v_mfma_scale_f32_16x16x128_f8f6f4 v[184:187], v[20:27], v[36:43], v[184:187], v220, v216 op_sel_hi:[0,0,0]
	v_mfma_scale_f32_16x16x128_f8f6f4 v[180:183], v[28:35], v[36:43], v[180:183], v220, v216 op_sel_hi:[0,0,0]
	v_mfma_scale_f32_16x16x128_f8f6f4 v[168:171], v[20:27], v[44:51], v[168:171], v220, v216 op_sel_hi:[0,0,0]
	v_mfma_scale_f32_16x16x128_f8f6f4 v[164:167], v[28:35], v[44:51], v[164:167], v220, v216 op_sel_hi:[0,0,0]
	v_mfma_scale_f32_16x16x128_f8f6f4 v[152:155], v[20:27], v[52:59], v[152:155], v220, v216 op_sel_hi:[0,0,0]
	v_mfma_scale_f32_16x16x128_f8f6f4 v[148:151], v[28:35], v[52:59], v[148:151], v220, v216 op_sel_hi:[0,0,0]
	v_mfma_scale_f32_16x16x128_f8f6f4 v[136:139], v[20:27], v[60:67], v[136:139], v220, v216 op_sel_hi:[0,0,0]
	v_mfma_scale_f32_16x16x128_f8f6f4 v[132:135], v[28:35], v[60:67], v[132:135], v220, v216 op_sel_hi:[0,0,0]
	s_setprio 0
	s_barrier
	s_add_i32 s66, s86, s8
	s_mov_b32 m0, s66
	ds_read_b128 v[36:39], v243 offset:49152
	ds_read_b128 v[40:43], v243 offset:50176
	ds_read_b128 v[44:47], v243 offset:51200
	ds_read_b128 v[48:51], v243 offset:52224
	ds_read_b128 v[52:55], v243 offset:53248
	ds_read_b128 v[56:59], v243 offset:54272
	ds_read_b128 v[60:63], v243 offset:55296
	ds_read_b128 v[64:67], v243 offset:56320
	v_lshl_add_u64 v[212:213], s[64:65], 0, v[198:199]
	global_load_lds_dwordx4 v[212:213], off
	s_add_i32 m0, s66, 0x2000
	s_add_u32 s62, s62, 0x8080
	v_lshl_add_u64 v[212:213], s[64:65], 0, v[196:197]
	s_addc_u32 s63, s63, 0
	s_add_i32 s64, s87, s8
	global_load_lds_dwordx4 v[212:213], off
	v_lshl_add_u64 v[212:213], s[62:63], 0, v[198:199]
	s_mov_b32 m0, s64
	s_nop 0
	global_load_lds_dwordx4 v[212:213], off
	v_lshl_add_u64 v[212:213], s[62:63], 0, v[196:197]
	s_add_i32 m0, s64, 0x2000
	s_nop 0
	global_load_lds_dwordx4 v[212:213], off
	s_mov_b32 m0, s69
	s_nop 0
	global_load_lds_dwordx4 v200, s[60:61]
	s_mov_b32 m0, s70
	s_nop 0
	global_load_lds_dwordx4 v202, s[60:61]
	s_waitcnt vmcnt(8)
	s_waitcnt lgkmcnt(0)
	s_barrier
	s_setprio 1
	s_waitcnt lgkmcnt(0)
	v_mfma_scale_f32_16x16x128_f8f6f4 v[128:131], v[4:11], v[36:43], v[128:131], v220, v216 op_sel_hi:[0,0,0]
	v_mfma_scale_f32_16x16x128_f8f6f4 v[124:127], v[12:19], v[36:43], v[124:127], v220, v216 op_sel_hi:[0,0,0]
	v_mfma_scale_f32_16x16x128_f8f6f4 v[112:115], v[4:11], v[44:51], v[112:115], v220, v216 op_sel_hi:[0,0,0]
	v_mfma_scale_f32_16x16x128_f8f6f4 v[108:111], v[12:19], v[44:51], v[108:111], v220, v216 op_sel_hi:[0,0,0]
	v_mfma_scale_f32_16x16x128_f8f6f4 v[96:99], v[4:11], v[52:59], v[96:99], v220, v216 op_sel_hi:[0,0,0]
	v_mfma_scale_f32_16x16x128_f8f6f4 v[92:95], v[12:19], v[52:59], v[92:95], v220, v216 op_sel_hi:[0,0,0]
	v_mfma_scale_f32_16x16x128_f8f6f4 v[80:83], v[4:11], v[60:67], v[80:83], v220, v216 op_sel_hi:[0,0,0]
	v_mfma_scale_f32_16x16x128_f8f6f4 v[76:79], v[12:19], v[60:67], v[76:79], v220, v216 op_sel_hi:[0,0,0]
	s_setprio 0
	s_setprio 1
	v_mfma_scale_f32_16x16x128_f8f6f4 v[120:123], v[20:27], v[36:43], v[120:123], v220, v216 op_sel_hi:[0,0,0]
	v_mfma_scale_f32_16x16x128_f8f6f4 v[116:119], v[28:35], v[36:43], v[116:119], v220, v216 op_sel_hi:[0,0,0]
	v_mfma_scale_f32_16x16x128_f8f6f4 v[104:107], v[20:27], v[44:51], v[104:107], v220, v216 op_sel_hi:[0,0,0]
	v_mfma_scale_f32_16x16x128_f8f6f4 v[100:103], v[28:35], v[44:51], v[100:103], v220, v216 op_sel_hi:[0,0,0]
	v_mfma_scale_f32_16x16x128_f8f6f4 v[88:91], v[20:27], v[52:59], v[88:91], v220, v216 op_sel_hi:[0,0,0]
	v_mfma_scale_f32_16x16x128_f8f6f4 v[84:87], v[28:35], v[52:59], v[84:87], v220, v216 op_sel_hi:[0,0,0]
	v_mfma_scale_f32_16x16x128_f8f6f4 v[72:75], v[20:27], v[60:67], v[72:75], v220, v216 op_sel_hi:[0,0,0]
	v_mfma_scale_f32_16x16x128_f8f6f4 v[68:71], v[28:35], v[60:67], v[68:71], v220, v216 op_sel_hi:[0,0,0]
	s_setprio 0
	s_barrier
	s_add_u32 s2, s2, 0x100
	s_addc_u32 s3, s3, 0
	s_cmp_ge_i32 s83, s5
	s_cbranch_scc1 .LBB0_775
.LBB0_772:
	ds_read_b128 v[20:23], v230
	ds_read_b128 v[24:27], v230 offset:1024
	ds_read_b128 v[28:31], v230 offset:2048
	ds_read_b128 v[32:35], v230 offset:3072
	ds_read_b128 v[4:7], v231
	ds_read_b128 v[8:11], v231 offset:1024
	ds_read_b128 v[12:15], v231 offset:2048
	ds_read_b128 v[16:19], v231 offset:3072
	s_cmp_eq_u32 s72, s83
	s_cselect_b64 s[62:63], -1, 0
	s_add_u32 s60, s42, s2
	s_addc_u32 s61, s43, s3
	s_add_u32 s60, s60, 0xffffff80
	s_addc_u32 s61, s61, -1
	s_add_i32 m0, s9, 0xc000
	s_add_i32 s64, s9, 0xe000
	s_cmp_lg_u32 s72, s83
	ds_read_b128 v[60:63], v243
	ds_read_b128 v[64:67], v243 offset:1024
	ds_read_b128 v[52:55], v243 offset:2048
	ds_read_b128 v[56:59], v243 offset:3072
	ds_read_b128 v[44:47], v243 offset:4096
	ds_read_b128 v[48:51], v243 offset:5120
	ds_read_b128 v[36:39], v243 offset:6144
	ds_read_b128 v[40:43], v243 offset:7168
	global_load_lds_dwordx4 v2, s[60:61]
	s_mov_b32 m0, s64
	s_nop 0
	global_load_lds_dwordx4 v204, s[60:61]
	s_cbranch_scc0 .LBB0_770
	v_mov_b32_e32 v205, v3
	v_mov_b64_e32 v[212:213], v[204:205]
	v_mov_b64_e32 v[214:215], v[2:3]
	s_cmp_eq_u32 s83, 0
	s_cbranch_scc1 .Lpeel_pi
	s_branch .LBB0_771

; #define PG8_STAGEA(bufoff, gbase, h) do { if constexpr (GATHER) { PG8_STAGE(bufoff, gbase, vA[h]); } else { PG8_STAGE(bufoff, (gbase) + (h) * hstepA, voffA); } } while (0)
; #define PG8_LDA(dst, b, h) do { _Pragma("unroll") for (int m = 0; m < 4; ++m) _Pragma("unroll") for (int k = 0; k < 2; ++k) dst[m][k] = *(const LAS bf16x8*)(lds + PG8_SA(b, h) + aoff + m * 2048 + k * 1024); } while (0)
; #define PG8_SCHED __builtin_amdgcn_sched_barrier(0)
; template <class Epi, class Sched>
; __device__ __forceinline__ void gemm_phase(const int tid, LAS unsigned char* lds, const char* Abase, const int lda, const int ldb, const int K, const Sched& S, const Epi& E) {
;     ...
; #pragma unroll 1
;         for (int t = 0; t < nt; t += 2) {
;             const bool last = (t == nt - 2);
;             const char* a1 = cA + (size_t)(t + 1) * kstepA;
;             const char* a2 = last ? nA : cA + (size_t)(t + 2) * kstepA; const char* b2 = last ? nB : cB + (size_t)(t + 2) * kstep;
;             const char* a3 = a2 + kstepA; const char* b3 = b2 + kstep;
;             PG8_LDB(B0, 0, 0); PG8_LDB(B1, 0, 1); PG8_SCHED; PG8_LDA(At, 0, 0); PG8_STAGEA(PG8_SA(1, 1), a1, 1);
.LBB0_1163:
	s_andn2_b64 vcc, exec, s[46:47]
	s_cbranch_vccnz .LBB0_1169
	v_mov_b32_e32 v207, v3
	v_mov_b32_e32 v209, v3
	s_mov_b32 s83, 0
	s_mov_b64 s[56:57], 0x100
	s_waitcnt lgkmcnt(0)
	v_add_u32_e32 v230, 0x10000, v199
	v_add_u32_e32 v231, 0x14000, v199
	v_add_u32_e32 v234, 0x18000, v199
	v_add_u32_e32 v235, 0x1c000, v199
	s_branch .LBB0_1167

; #define PG8_STAGEA(bufoff, gbase, h) do { if constexpr (GATHER) { PG8_STAGE(bufoff, gbase, vA[h]); } else { PG8_STAGE(bufoff, (gbase) + (h) * hstepA, voffA); } } while (0)
; #define PG8_LDA(dst, b, h) do { _Pragma("unroll") for (int m = 0; m < 4; ++m) _Pragma("unroll") for (int k = 0; k < 2; ++k) dst[m][k] = *(const LAS bf16x8*)(lds + PG8_SA(b, h) + aoff + m * 2048 + k * 1024); } while (0)
; #define PG8_MM(ai, bj, At, Bt) do { if constexpr (Epi::F8MMA) PG8_MMA8(ai, bj, At, Bt##8); else PG8_MMA(ai, bj, At, Bt); } while (0)
; #define PG8_WAIT_V(n) asm volatile("s_waitcnt vmcnt(" #n ")" ::: "memory")
; #define PG8_WAIT_L(n) asm volatile("s_waitcnt lgkmcnt(" #n ")" ::: "memory")
; #define PG8_BAR __builtin_amdgcn_s_barrier()
; #define PG8_SCHED __builtin_amdgcn_sched_barrier(0)
; template <class Epi, class Sched>
; __device__ __forceinline__ void gemm_phase(const int tid, LAS unsigned char* lds, const char* Abase, const int lda, const int ldb, const int K, const Sched& S, const Epi& E) {
;     ...
;             PG8_WAIT_V(8); PG8_WAIT_L(0); PG8_BAR; PG8_MM(0, 0, At, B0); PG8_MM(0, 1, At, B1); PG8_BAR; PG8_SCHED;
;             PG8_LDA(At, 0, 1); PG8_STAGE(PG8_SB(0, 0), b2, voffB); PG8_STAGE(PG8_SB(0, 1), b2 + hstepB, voffB); PG8_STAGEA(PG8_SA(0, 0), a2, 0);
;             PG8_WAIT_V(8); PG8_WAIT_L(0); PG8_BAR; PG8_MM(1, 0, At, B0); PG8_MM(1, 1, At, B1); PG8_BAR; PG8_SCHED;
.LBB0_1166:
	s_add_i32 s83, s83, 2
	s_and_b64 s[60:61], s[62:63], exec
	s_cselect_b32 s61, 0, s56
	s_cselect_b32 s60, 0, s57
	s_add_u32 s66, s40, s61
	s_addc_u32 s67, s41, s60
	s_add_u32 s64, s54, s56
	s_addc_u32 s65, s55, s57
	s_add_u32 s60, s66, 0x80
	s_addc_u32 s61, s67, 0
	s_waitcnt vmcnt(8)
	s_and_b64 s[62:63], s[62:63], exec
	s_waitcnt lgkmcnt(0)
	s_cselect_b32 s62, s52, s64
	s_cselect_b32 s63, s53, s65
	s_add_u32 s64, s62, 0x80
	s_addc_u32 s65, s63, 0
	s_barrier
	s_setprio 1
	s_waitcnt lgkmcnt(0)
	v_mfma_scale_f32_16x16x128_f8f6f4 v[192:195], v[20:27], v[60:67], v[192:195], v221, v216 op_sel_hi:[0,0,0]
	v_mfma_scale_f32_16x16x128_f8f6f4 v[188:191], v[28:35], v[60:67], v[188:191], v221, v216 op_sel_hi:[0,0,0]
	v_mfma_scale_f32_16x16x128_f8f6f4 v[176:179], v[20:27], v[52:59], v[176:179], v221, v216 op_sel_hi:[0,0,0]
	v_mfma_scale_f32_16x16x128_f8f6f4 v[172:175], v[28:35], v[52:59], v[172:175], v221, v216 op_sel_hi:[0,0,0]
	v_mfma_scale_f32_16x16x128_f8f6f4 v[160:163], v[20:27], v[44:51], v[160:163], v221, v216 op_sel_hi:[0,0,0]
	v_mfma_scale_f32_16x16x128_f8f6f4 v[156:159], v[28:35], v[44:51], v[156:159], v221, v216 op_sel_hi:[0,0,0]
	v_mfma_scale_f32_16x16x128_f8f6f4 v[144:147], v[20:27], v[36:43], v[144:147], v221, v216 op_sel_hi:[0,0,0]
	v_mfma_scale_f32_16x16x128_f8f6f4 v[140:143], v[28:35], v[36:43], v[140:143], v221, v216 op_sel_hi:[0,0,0]
	s_setprio 0
	s_setprio 1
	v_mfma_scale_f32_16x16x128_f8f6f4 v[184:187], v[4:11], v[60:67], v[184:187], v221, v216 op_sel_hi:[0,0,0]
	v_mfma_scale_f32_16x16x128_f8f6f4 v[180:183], v[12:19], v[60:67], v[180:183], v221, v216 op_sel_hi:[0,0,0]
	v_mfma_scale_f32_16x16x128_f8f6f4 v[168:171], v[4:11], v[52:59], v[168:171], v221, v216 op_sel_hi:[0,0,0]
	v_mfma_scale_f32_16x16x128_f8f6f4 v[164:167], v[12:19], v[52:59], v[164:167], v221, v216 op_sel_hi:[0,0,0]
	v_mfma_scale_f32_16x16x128_f8f6f4 v[152:155], v[4:11], v[44:51], v[152:155], v221, v216 op_sel_hi:[0,0,0]
	v_mfma_scale_f32_16x16x128_f8f6f4 v[148:151], v[12:19], v[44:51], v[148:151], v221, v216 op_sel_hi:[0,0,0]
	v_mfma_scale_f32_16x16x128_f8f6f4 v[136:139], v[4:11], v[36:43], v[136:139], v221, v216 op_sel_hi:[0,0,0]
	v_mfma_scale_f32_16x16x128_f8f6f4 v[132:135], v[12:19], v[36:43], v[132:135], v221, v216 op_sel_hi:[0,0,0]
	s_setprio 0
	s_barrier
	s_mov_b32 m0, s10
	s_add_u32 s86, s62, 0x8000
	ds_read_b128 v[36:39], v243 offset:16384
	ds_read_b128 v[40:43], v243 offset:17408
	ds_read_b128 v[44:47], v243 offset:18432
	ds_read_b128 v[48:51], v243 offset:19456
	ds_read_b128 v[52:55], v243 offset:20480
	ds_read_b128 v[56:59], v243 offset:21504
	ds_read_b128 v[60:63], v243 offset:22528
	ds_read_b128 v[64:67], v243 offset:23552
	v_lshl_add_u64 v[228:229], s[62:63], 0, v[196:197]
	global_load_lds_dwordx4 v[228:229], off
	v_lshl_add_u64 v[228:229], s[62:63], 0, v[0:1]
	s_mov_b32 m0, s11
	s_addc_u32 s87, s63, 0
	global_load_lds_dwordx4 v[228:229], off
	v_lshl_add_u64 v[228:229], s[86:87], 0, v[196:197]
	s_mov_b32 m0, s22
	s_nop 0
	global_load_lds_dwordx4 v[228:229], off
	v_lshl_add_u64 v[228:229], s[86:87], 0, v[0:1]
	s_mov_b32 m0, s25
	s_nop 0
	global_load_lds_dwordx4 v[228:229], off
	s_mov_b32 m0, s9
	s_nop 0
	global_load_lds_dwordx4 v198, s[66:67]
	s_mov_b32 m0, s28
	s_nop 0
	global_load_lds_dwordx4 v200, s[66:67]
	s_waitcnt vmcnt(8)
	s_waitcnt lgkmcnt(0)
	s_barrier
	s_setprio 1
	s_waitcnt lgkmcnt(0)
	v_mfma_scale_f32_16x16x128_f8f6f4 v[128:131], v[20:27], v[36:43], v[128:131], v221, v216 op_sel_hi:[0,0,0]
	v_mfma_scale_f32_16x16x128_f8f6f4 v[124:127], v[28:35], v[36:43], v[124:127], v221, v216 op_sel_hi:[0,0,0]
	v_mfma_scale_f32_16x16x128_f8f6f4 v[112:115], v[20:27], v[44:51], v[112:115], v221, v216 op_sel_hi:[0,0,0]
	v_mfma_scale_f32_16x16x128_f8f6f4 v[108:111], v[28:35], v[44:51], v[108:111], v221, v216 op_sel_hi:[0,0,0]
	v_mfma_scale_f32_16x16x128_f8f6f4 v[96:99], v[20:27], v[52:59], v[96:99], v221, v216 op_sel_hi:[0,0,0]
	v_mfma_scale_f32_16x16x128_f8f6f4 v[92:95], v[28:35], v[52:59], v[92:95], v221, v216 op_sel_hi:[0,0,0]
	v_mfma_scale_f32_16x16x128_f8f6f4 v[80:83], v[20:27], v[60:67], v[80:83], v221, v216 op_sel_hi:[0,0,0]
	v_mfma_scale_f32_16x16x128_f8f6f4 v[76:79], v[28:35], v[60:67], v[76:79], v221, v216 op_sel_hi:[0,0,0]
	s_setprio 0
	s_setprio 1
	v_mfma_scale_f32_16x16x128_f8f6f4 v[120:123], v[4:11], v[36:43], v[120:123], v221, v216 op_sel_hi:[0,0,0]
	v_mfma_scale_f32_16x16x128_f8f6f4 v[116:119], v[12:19], v[36:43], v[116:119], v221, v216 op_sel_hi:[0,0,0]
	v_mfma_scale_f32_16x16x128_f8f6f4 v[104:107], v[4:11], v[44:51], v[104:107], v221, v216 op_sel_hi:[0,0,0]
	v_mfma_scale_f32_16x16x128_f8f6f4 v[100:103], v[12:19], v[44:51], v[100:103], v221, v216 op_sel_hi:[0,0,0]
	v_mfma_scale_f32_16x16x128_f8f6f4 v[88:91], v[4:11], v[52:59], v[88:91], v221, v216 op_sel_hi:[0,0,0]
	v_mfma_scale_f32_16x16x128_f8f6f4 v[84:87], v[12:19], v[52:59], v[84:87], v221, v216 op_sel_hi:[0,0,0]
	v_mfma_scale_f32_16x16x128_f8f6f4 v[72:75], v[4:11], v[60:67], v[72:75], v221, v216 op_sel_hi:[0,0,0]
	v_mfma_scale_f32_16x16x128_f8f6f4 v[68:71], v[12:19], v[60:67], v[68:71], v221, v216 op_sel_hi:[0,0,0]
	s_setprio 0
	s_barrier
; #define PG8_STAGEA(bufoff, gbase, h) do { if constexpr (GATHER) { PG8_STAGE(bufoff, gbase, vA[h]); } else { PG8_STAGE(bufoff, (gbase) + (h) * hstepA, voffA); } } while (0)
; #define PG8_LDA(dst, b, h) do { _Pragma("unroll") for (int m = 0; m < 4; ++m) _Pragma("unroll") for (int k = 0; k < 2; ++k) dst[m][k] = *(const LAS bf16x8*)(lds + PG8_SA(b, h) + aoff + m * 2048 + k * 1024); } while (0)
; #define PG8_MM(ai, bj, At, Bt) do { if constexpr (Epi::F8MMA) PG8_MMA8(ai, bj, At, Bt##8); else PG8_MMA(ai, bj, At, Bt); } while (0)
; #define PG8_WAIT_V(n) asm volatile("s_waitcnt vmcnt(" #n ")" ::: "memory")
; #define PG8_WAIT_L(n) asm volatile("s_waitcnt lgkmcnt(" #n ")" ::: "memory")
; #define PG8_BAR __builtin_amdgcn_s_barrier()
; #define PG8_SCHED __builtin_amdgcn_sched_barrier(0)
; template <class Epi, class Sched>
; __device__ __forceinline__ void gemm_phase(const int tid, LAS unsigned char* lds, const char* Abase, const int lda, const int ldb, const int K, const Sched& S, const Epi& E) {
;     ...
;             PG8_LDB(B0, 0, 0); PG8_LDB(B1, 0, 1); PG8_SCHED; PG8_LDA(At, 0, 0); PG8_STAGEA(PG8_SA(1, 1), a1, 1);
;     ...
;             PG8_LDA(At, 0, 1); PG8_STAGE(PG8_SB(0, 0), b2, voffB); PG8_STAGE(PG8_SB(0, 1), b2 + hstepB, voffB); PG8_STAGEA(PG8_SA(0, 0), a2, 0);
;             PG8_WAIT_V(8); PG8_WAIT_L(0); PG8_BAR; PG8_MM(1, 0, At, B0); PG8_MM(1, 1, At, B1); PG8_BAR; PG8_SCHED;
;             PG8_LDB(B0, 1, 0); PG8_LDB(B1, 1, 1); PG8_SCHED; PG8_LDA(At, 1, 0); PG8_STAGEA(PG8_SA(0, 1), a2, 1);
;             PG8_WAIT_V(8); PG8_WAIT_L(0); PG8_BAR; PG8_MM(0, 0, At, B0); PG8_MM(0, 1, At, B1); PG8_BAR; PG8_SCHED;
;             PG8_LDA(At, 1, 1); PG8_STAGE(PG8_SB(1, 0), b3, voffB); PG8_STAGE(PG8_SB(1, 1), b3 + hstepB, voffB); PG8_STAGEA(PG8_SA(1, 0), a3, 0);
;             PG8_WAIT_V(8); PG8_WAIT_L(0); PG8_BAR; PG8_MM(1, 0, At, B0); PG8_MM(1, 1, At, B1); PG8_BAR; PG8_SCHED;
.Lmid_po:
	s_add_i32 s86, 0, 0x18000
	s_add_i32 s87, 0, 0x1c000
	ds_read_b128 v[4:7], v234
	ds_read_b128 v[8:11], v234 offset:1024
	ds_read_b128 v[12:15], v234 offset:2048
	ds_read_b128 v[16:19], v234 offset:3072
	ds_read_b128 v[20:23], v235
	ds_read_b128 v[24:27], v235 offset:1024
	ds_read_b128 v[28:31], v235 offset:2048
	ds_read_b128 v[32:35], v235 offset:3072
	s_mov_b32 m0, s29
	ds_read_b128 v[36:39], v243 offset:32768
	ds_read_b128 v[40:43], v243 offset:33792
	ds_read_b128 v[44:47], v243 offset:34816
	ds_read_b128 v[48:51], v243 offset:35840
	ds_read_b128 v[52:55], v243 offset:36864
	ds_read_b128 v[56:59], v243 offset:37888
	ds_read_b128 v[60:63], v243 offset:38912
	ds_read_b128 v[64:67], v243 offset:39936
	v_lshl_add_u64 v[212:213], s[66:67], 0, v[212:213]
	global_load_lds_dwordx4 v[212:213], off
	v_lshl_add_u64 v[210:211], s[66:67], 0, v[210:211]
	s_mov_b32 m0, s68
	s_nop 0
	global_load_lds_dwordx4 v[210:211], off
	s_waitcnt vmcnt(8)
	s_waitcnt lgkmcnt(0)
	s_barrier
	s_setprio 1
	s_waitcnt lgkmcnt(0)
	v_mfma_scale_f32_16x16x128_f8f6f4 v[192:195], v[4:11], v[36:43], v[192:195], v221, v216 op_sel_hi:[0,0,0]
	v_mfma_scale_f32_16x16x128_f8f6f4 v[188:191], v[12:19], v[36:43], v[188:191], v221, v216 op_sel_hi:[0,0,0]
	v_mfma_scale_f32_16x16x128_f8f6f4 v[176:179], v[4:11], v[44:51], v[176:179], v221, v216 op_sel_hi:[0,0,0]
	v_mfma_scale_f32_16x16x128_f8f6f4 v[172:175], v[12:19], v[44:51], v[172:175], v221, v216 op_sel_hi:[0,0,0]
	v_mfma_scale_f32_16x16x128_f8f6f4 v[160:163], v[4:11], v[52:59], v[160:163], v221, v216 op_sel_hi:[0,0,0]
	v_mfma_scale_f32_16x16x128_f8f6f4 v[156:159], v[12:19], v[52:59], v[156:159], v221, v216 op_sel_hi:[0,0,0]
	v_mfma_scale_f32_16x16x128_f8f6f4 v[144:147], v[4:11], v[60:67], v[144:147], v221, v216 op_sel_hi:[0,0,0]
	v_mfma_scale_f32_16x16x128_f8f6f4 v[140:143], v[12:19], v[60:67], v[140:143], v221, v216 op_sel_hi:[0,0,0]
	s_setprio 0
	s_setprio 1
	v_mfma_scale_f32_16x16x128_f8f6f4 v[184:187], v[20:27], v[36:43], v[184:187], v221, v216 op_sel_hi:[0,0,0]
	v_mfma_scale_f32_16x16x128_f8f6f4 v[180:183], v[28:35], v[36:43], v[180:183], v221, v216 op_sel_hi:[0,0,0]
	v_mfma_scale_f32_16x16x128_f8f6f4 v[168:171], v[20:27], v[44:51], v[168:171], v221, v216 op_sel_hi:[0,0,0]
	v_mfma_scale_f32_16x16x128_f8f6f4 v[164:167], v[28:35], v[44:51], v[164:167], v221, v216 op_sel_hi:[0,0,0]
	v_mfma_scale_f32_16x16x128_f8f6f4 v[152:155], v[20:27], v[52:59], v[152:155], v221, v216 op_sel_hi:[0,0,0]
	v_mfma_scale_f32_16x16x128_f8f6f4 v[148:151], v[28:35], v[52:59], v[148:151], v221, v216 op_sel_hi:[0,0,0]
	v_mfma_scale_f32_16x16x128_f8f6f4 v[136:139], v[20:27], v[60:67], v[136:139], v221, v216 op_sel_hi:[0,0,0]
	v_mfma_scale_f32_16x16x128_f8f6f4 v[132:135], v[28:35], v[60:67], v[132:135], v221, v216 op_sel_hi:[0,0,0]
	s_setprio 0
	s_barrier
	s_add_i32 s66, s86, s8
	s_mov_b32 m0, s66
	ds_read_b128 v[36:39], v243 offset:49152
	ds_read_b128 v[40:43], v243 offset:50176
	ds_read_b128 v[44:47], v243 offset:51200
	ds_read_b128 v[48:51], v243 offset:52224
	ds_read_b128 v[52:55], v243 offset:53248
	ds_read_b128 v[56:59], v243 offset:54272
	ds_read_b128 v[60:63], v243 offset:55296
	ds_read_b128 v[64:67], v243 offset:56320
	v_lshl_add_u64 v[210:211], s[64:65], 0, v[196:197]
	global_load_lds_dwordx4 v[210:211], off
	s_add_i32 m0, s66, 0x2000
	s_add_u32 s62, s62, 0x8080
	v_lshl_add_u64 v[210:211], s[64:65], 0, v[0:1]
	s_addc_u32 s63, s63, 0
	s_add_i32 s64, s87, s8
	global_load_lds_dwordx4 v[210:211], off
	v_lshl_add_u64 v[210:211], s[62:63], 0, v[196:197]
	s_mov_b32 m0, s64
	s_nop 0
	global_load_lds_dwordx4 v[210:211], off
	v_lshl_add_u64 v[210:211], s[62:63], 0, v[0:1]
	s_add_i32 m0, s64, 0x2000
	s_nop 0
	global_load_lds_dwordx4 v[210:211], off
	s_mov_b32 m0, s69
	s_nop 0
	global_load_lds_dwordx4 v198, s[60:61]
	s_mov_b32 m0, s70
	s_nop 0
	global_load_lds_dwordx4 v200, s[60:61]
	s_waitcnt vmcnt(8)
	s_waitcnt lgkmcnt(0)
	s_barrier
	s_setprio 1
	s_waitcnt lgkmcnt(0)
	v_mfma_scale_f32_16x16x128_f8f6f4 v[128:131], v[4:11], v[36:43], v[128:131], v221, v216 op_sel_hi:[0,0,0]
	v_mfma_scale_f32_16x16x128_f8f6f4 v[124:127], v[12:19], v[36:43], v[124:127], v221, v216 op_sel_hi:[0,0,0]
	v_mfma_scale_f32_16x16x128_f8f6f4 v[112:115], v[4:11], v[44:51], v[112:115], v221, v216 op_sel_hi:[0,0,0]
	v_mfma_scale_f32_16x16x128_f8f6f4 v[108:111], v[12:19], v[44:51], v[108:111], v221, v216 op_sel_hi:[0,0,0]
	v_mfma_scale_f32_16x16x128_f8f6f4 v[96:99], v[4:11], v[52:59], v[96:99], v221, v216 op_sel_hi:[0,0,0]
	v_mfma_scale_f32_16x16x128_f8f6f4 v[92:95], v[12:19], v[52:59], v[92:95], v221, v216 op_sel_hi:[0,0,0]
	v_mfma_scale_f32_16x16x128_f8f6f4 v[80:83], v[4:11], v[60:67], v[80:83], v221, v216 op_sel_hi:[0,0,0]
	v_mfma_scale_f32_16x16x128_f8f6f4 v[76:79], v[12:19], v[60:67], v[76:79], v221, v216 op_sel_hi:[0,0,0]
	s_setprio 0
	s_setprio 1
	v_mfma_scale_f32_16x16x128_f8f6f4 v[120:123], v[20:27], v[36:43], v[120:123], v221, v216 op_sel_hi:[0,0,0]
	v_mfma_scale_f32_16x16x128_f8f6f4 v[116:119], v[28:35], v[36:43], v[116:119], v221, v216 op_sel_hi:[0,0,0]
	v_mfma_scale_f32_16x16x128_f8f6f4 v[104:107], v[20:27], v[44:51], v[104:107], v221, v216 op_sel_hi:[0,0,0]
	v_mfma_scale_f32_16x16x128_f8f6f4 v[100:103], v[28:35], v[44:51], v[100:103], v221, v216 op_sel_hi:[0,0,0]
	v_mfma_scale_f32_16x16x128_f8f6f4 v[88:91], v[20:27], v[52:59], v[88:91], v221, v216 op_sel_hi:[0,0,0]
	v_mfma_scale_f32_16x16x128_f8f6f4 v[84:87], v[28:35], v[52:59], v[84:87], v221, v216 op_sel_hi:[0,0,0]
	v_mfma_scale_f32_16x16x128_f8f6f4 v[72:75], v[20:27], v[60:67], v[72:75], v221, v216 op_sel_hi:[0,0,0]
	v_mfma_scale_f32_16x16x128_f8f6f4 v[68:71], v[28:35], v[60:67], v[68:71], v221, v216 op_sel_hi:[0,0,0]
	s_setprio 0
	s_barrier
	s_add_u32 s56, s56, 0x100
	s_addc_u32 s57, s57, 0
	s_cmp_ge_i32 s83, s5
	s_cbranch_scc1 .LBB0_1170
.LBB0_1167:
	ds_read_b128 v[20:23], v230
	ds_read_b128 v[24:27], v230 offset:1024
	ds_read_b128 v[28:31], v230 offset:2048
	ds_read_b128 v[32:35], v230 offset:3072
	ds_read_b128 v[4:7], v231
	ds_read_b128 v[8:11], v231 offset:1024
	ds_read_b128 v[12:15], v231 offset:2048
	ds_read_b128 v[16:19], v231 offset:3072
	s_cmp_eq_u32 s72, s83
	s_cselect_b64 s[62:63], -1, 0
	s_add_u32 s60, s40, s56
	s_addc_u32 s61, s41, s57
	s_add_u32 s60, s60, 0xffffff80
	s_addc_u32 s61, s61, -1
	s_add_i32 m0, s9, 0xc000
	s_add_i32 s64, s9, 0xe000
	s_cmp_lg_u32 s72, s83
	ds_read_b128 v[60:63], v243
	ds_read_b128 v[64:67], v243 offset:1024
	ds_read_b128 v[52:55], v243 offset:2048
	ds_read_b128 v[56:59], v243 offset:3072
	ds_read_b128 v[44:47], v243 offset:4096
	ds_read_b128 v[48:51], v243 offset:5120
	ds_read_b128 v[36:39], v243 offset:6144
	ds_read_b128 v[40:43], v243 offset:7168
	global_load_lds_dwordx4 v2, s[60:61]
	s_mov_b32 m0, s64
	s_nop 0
	global_load_lds_dwordx4 v202, s[60:61]
	s_cbranch_scc0 .LBB0_1165
	v_mov_b32_e32 v203, v3
	v_mov_b64_e32 v[210:211], v[202:203]
	v_mov_b64_e32 v[212:213], v[2:3]
	s_cmp_eq_u32 s83, 0
	s_cbranch_scc1 .Lpeel_po
	s_branch .LBB0_1166

; #define PG8_STAGEA(bufoff, gbase, h) do { if constexpr (GATHER) { PG8_STAGE(bufoff, gbase, vA[h]); } else { PG8_STAGE(bufoff, (gbase) + (h) * hstepA, voffA); } } while (0)
; #define PG8_LDA(dst, b, h) do { _Pragma("unroll") for (int m = 0; m < 4; ++m) _Pragma("unroll") for (int k = 0; k < 2; ++k) dst[m][k] = *(const LAS bf16x8*)(lds + PG8_SA(b, h) + aoff + m * 2048 + k * 1024); } while (0)
; #define PG8_SCHED __builtin_amdgcn_sched_barrier(0)
; template <class Epi, class Sched>
; __device__ __forceinline__ void gemm_phase(const int tid, LAS unsigned char* lds, const char* Abase, const int lda, const int ldb, const int K, const Sched& S, const Epi& E) {
;     ...
; #pragma unroll 1
;         for (int t = 0; t < nt; t += 2) {
;             const bool last = (t == nt - 2);
;             const char* a1 = cA + (size_t)(t + 1) * kstepA;
;             const char* a2 = last ? nA : cA + (size_t)(t + 2) * kstepA; const char* b2 = last ? nB : cB + (size_t)(t + 2) * kstep;
;             const char* a3 = a2 + kstepA; const char* b3 = b2 + kstep;
;             PG8_LDB(B0, 0, 0); PG8_LDB(B1, 0, 1); PG8_SCHED; PG8_LDA(At, 0, 0); PG8_STAGEA(PG8_SA(1, 1), a1, 1);
.LBB0_1592:
	s_waitcnt vmcnt(0)
	s_andn2_b64 vcc, exec, s[50:51]
	s_cbranch_vccnz .LBB0_1598
	v_mov_b32_e32 v209, v3
	v_mov_b32_e32 v211, v3
	s_mov_b32 s41, 0
	s_mov_b64 s[62:63], 0x100
	v_add_u32_e32 v230, 0x10000, v1
	v_add_u32_e32 v231, 0x14000, v1
	v_add_u32_e32 v234, 0x18000, v1
	v_add_u32_e32 v235, 0x1c000, v1
	s_branch .LBB0_1596

; #define PG8_STAGEA(bufoff, gbase, h) do { if constexpr (GATHER) { PG8_STAGE(bufoff, gbase, vA[h]); } else { PG8_STAGE(bufoff, (gbase) + (h) * hstepA, voffA); } } while (0)
; #define PG8_LDA(dst, b, h) do { _Pragma("unroll") for (int m = 0; m < 4; ++m) _Pragma("unroll") for (int k = 0; k < 2; ++k) dst[m][k] = *(const LAS bf16x8*)(lds + PG8_SA(b, h) + aoff + m * 2048 + k * 1024); } while (0)
; #define PG8_MM(ai, bj, At, Bt) do { if constexpr (Epi::F8MMA) PG8_MMA8(ai, bj, At, Bt##8); else PG8_MMA(ai, bj, At, Bt); } while (0)
; #define PG8_WAIT_V(n) asm volatile("s_waitcnt vmcnt(" #n ")" ::: "memory")
; #define PG8_WAIT_L(n) asm volatile("s_waitcnt lgkmcnt(" #n ")" ::: "memory")
; #define PG8_BAR __builtin_amdgcn_s_barrier()
; #define PG8_SCHED __builtin_amdgcn_sched_barrier(0)
; template <class Epi, class Sched>
; __device__ __forceinline__ void gemm_phase(const int tid, LAS unsigned char* lds, const char* Abase, const int lda, const int ldb, const int K, const Sched& S, const Epi& E) {
;     ...
;             PG8_WAIT_V(8); PG8_WAIT_L(0); PG8_BAR; PG8_MM(0, 0, At, B0); PG8_MM(0, 1, At, B1); PG8_BAR; PG8_SCHED;
;             PG8_LDA(At, 0, 1); PG8_STAGE(PG8_SB(0, 0), b2, voffB); PG8_STAGE(PG8_SB(0, 1), b2 + hstepB, voffB); PG8_STAGEA(PG8_SA(0, 0), a2, 0);
;             PG8_WAIT_V(8); PG8_WAIT_L(0); PG8_BAR; PG8_MM(1, 0, At, B0); PG8_MM(1, 1, At, B1); PG8_BAR; PG8_SCHED;
.LBB0_1595:
	s_add_i32 s41, s41, 2
	s_and_b64 s[64:65], s[66:67], exec
	s_cselect_b32 s65, 0, s62
	s_cselect_b32 s64, 0, s63
	s_add_u32 s70, s46, s65
	s_addc_u32 s71, s47, s64
	s_add_u32 s68, s42, s62
	s_addc_u32 s69, s43, s63
	s_add_u32 s64, s70, 0x80
	s_addc_u32 s65, s71, 0
	s_waitcnt vmcnt(8)
	s_and_b64 s[66:67], s[66:67], exec
	s_waitcnt lgkmcnt(0)
	s_cselect_b32 s66, s0, s68
	s_cselect_b32 s67, s1, s69
	s_add_u32 s68, s66, 0x80
	s_addc_u32 s69, s67, 0
	s_barrier
	s_setprio 1
	s_waitcnt lgkmcnt(0)
	v_mfma_scale_f32_16x16x128_f8f6f4 v[192:195], v[20:27], v[60:67], v[192:195], v220, v216 op_sel_hi:[0,0,0]
	v_mfma_scale_f32_16x16x128_f8f6f4 v[188:191], v[28:35], v[60:67], v[188:191], v220, v216 op_sel_hi:[0,0,0]
	v_mfma_scale_f32_16x16x128_f8f6f4 v[184:187], v[20:27], v[52:59], v[184:187], v220, v216 op_sel_hi:[0,0,0]
	v_mfma_scale_f32_16x16x128_f8f6f4 v[180:183], v[28:35], v[52:59], v[180:183], v220, v216 op_sel_hi:[0,0,0]
	v_mfma_scale_f32_16x16x128_f8f6f4 v[176:179], v[20:27], v[44:51], v[176:179], v220, v216 op_sel_hi:[0,0,0]
	v_mfma_scale_f32_16x16x128_f8f6f4 v[172:175], v[28:35], v[44:51], v[172:175], v220, v216 op_sel_hi:[0,0,0]
	v_mfma_scale_f32_16x16x128_f8f6f4 v[168:171], v[20:27], v[36:43], v[168:171], v220, v216 op_sel_hi:[0,0,0]
	v_mfma_scale_f32_16x16x128_f8f6f4 v[164:167], v[28:35], v[36:43], v[164:167], v220, v216 op_sel_hi:[0,0,0]
	s_setprio 0
	s_setprio 1
	v_mfma_scale_f32_16x16x128_f8f6f4 v[160:163], v[4:11], v[60:67], v[160:163], v216, v216 op_sel_hi:[0,0,0]
	v_mfma_scale_f32_16x16x128_f8f6f4 v[156:159], v[12:19], v[60:67], v[156:159], v216, v216 op_sel_hi:[0,0,0]
	v_mfma_scale_f32_16x16x128_f8f6f4 v[152:155], v[4:11], v[52:59], v[152:155], v216, v216 op_sel_hi:[0,0,0]
	v_mfma_scale_f32_16x16x128_f8f6f4 v[148:151], v[12:19], v[52:59], v[148:151], v216, v216 op_sel_hi:[0,0,0]
	v_mfma_scale_f32_16x16x128_f8f6f4 v[144:147], v[4:11], v[44:51], v[144:147], v216, v216 op_sel_hi:[0,0,0]
	v_mfma_scale_f32_16x16x128_f8f6f4 v[140:143], v[12:19], v[44:51], v[140:143], v216, v216 op_sel_hi:[0,0,0]
	v_mfma_scale_f32_16x16x128_f8f6f4 v[136:139], v[4:11], v[36:43], v[136:139], v216, v216 op_sel_hi:[0,0,0]
	v_mfma_scale_f32_16x16x128_f8f6f4 v[132:135], v[12:19], v[36:43], v[132:135], v216, v216 op_sel_hi:[0,0,0]
	s_setprio 0
	s_barrier
	s_mov_b32 m0, s76
	s_add_u32 vcc_lo, s66, 0x20000
	ds_read_b128 v[36:39], v244 offset:16384
	ds_read_b128 v[40:43], v244 offset:17408
	ds_read_b128 v[44:47], v244 offset:18432
	ds_read_b128 v[48:51], v244 offset:19456
	ds_read_b128 v[52:55], v244 offset:20480
	ds_read_b128 v[56:59], v244 offset:21504
	ds_read_b128 v[60:63], v244 offset:22528
	ds_read_b128 v[64:67], v244 offset:23552
	v_lshl_add_u64 v[228:229], s[66:67], 0, v[198:199]
	global_load_lds_dwordx4 v[228:229], off
	v_lshl_add_u64 v[228:229], s[66:67], 0, v[200:201]
	s_mov_b32 m0, s77
	s_addc_u32 vcc_hi, s67, 0
	global_load_lds_dwordx4 v[228:229], off
	v_lshl_add_u64 v[228:229], vcc, 0, v[198:199]
	s_mov_b32 m0, s78
	s_nop 0
	global_load_lds_dwordx4 v[228:229], off
	v_lshl_add_u64 v[228:229], vcc, 0, v[200:201]
	s_mov_b32 m0, s79
	s_nop 0
	global_load_lds_dwordx4 v[228:229], off
	s_mov_b32 m0, s73
	s_nop 0
	global_load_lds_dwordx4 v196, s[70:71]
	s_mov_b32 m0, s82
	s_nop 0
	global_load_lds_dwordx4 v0, s[70:71]
	s_waitcnt vmcnt(8)
	s_waitcnt lgkmcnt(0)
	s_barrier
	s_setprio 1
	s_waitcnt lgkmcnt(0)
	v_mfma_scale_f32_16x16x128_f8f6f4 v[128:131], v[20:27], v[36:43], v[128:131], v220, v216 op_sel_hi:[0,0,0]
	v_mfma_scale_f32_16x16x128_f8f6f4 v[124:127], v[28:35], v[36:43], v[124:127], v220, v216 op_sel_hi:[0,0,0]
	v_mfma_scale_f32_16x16x128_f8f6f4 v[120:123], v[20:27], v[44:51], v[120:123], v220, v216 op_sel_hi:[0,0,0]
	v_mfma_scale_f32_16x16x128_f8f6f4 v[116:119], v[28:35], v[44:51], v[116:119], v220, v216 op_sel_hi:[0,0,0]
	v_mfma_scale_f32_16x16x128_f8f6f4 v[112:115], v[20:27], v[52:59], v[112:115], v220, v216 op_sel_hi:[0,0,0]
	v_mfma_scale_f32_16x16x128_f8f6f4 v[108:111], v[28:35], v[52:59], v[108:111], v220, v216 op_sel_hi:[0,0,0]
	v_mfma_scale_f32_16x16x128_f8f6f4 v[104:107], v[20:27], v[60:67], v[104:107], v220, v216 op_sel_hi:[0,0,0]
	v_mfma_scale_f32_16x16x128_f8f6f4 v[100:103], v[28:35], v[60:67], v[100:103], v220, v216 op_sel_hi:[0,0,0]
	s_setprio 0
	s_setprio 1
	v_mfma_scale_f32_16x16x128_f8f6f4 v[96:99], v[4:11], v[36:43], v[96:99], v216, v216 op_sel_hi:[0,0,0]
	v_mfma_scale_f32_16x16x128_f8f6f4 v[92:95], v[12:19], v[36:43], v[92:95], v216, v216 op_sel_hi:[0,0,0]
	v_mfma_scale_f32_16x16x128_f8f6f4 v[88:91], v[4:11], v[44:51], v[88:91], v216, v216 op_sel_hi:[0,0,0]
	v_mfma_scale_f32_16x16x128_f8f6f4 v[84:87], v[12:19], v[44:51], v[84:87], v216, v216 op_sel_hi:[0,0,0]
	v_mfma_scale_f32_16x16x128_f8f6f4 v[80:83], v[4:11], v[52:59], v[80:83], v216, v216 op_sel_hi:[0,0,0]
	v_mfma_scale_f32_16x16x128_f8f6f4 v[76:79], v[12:19], v[52:59], v[76:79], v216, v216 op_sel_hi:[0,0,0]
	v_mfma_scale_f32_16x16x128_f8f6f4 v[72:75], v[4:11], v[60:67], v[72:75], v216, v216 op_sel_hi:[0,0,0]
	v_mfma_scale_f32_16x16x128_f8f6f4 v[68:71], v[12:19], v[60:67], v[68:71], v216, v216 op_sel_hi:[0,0,0]
	s_setprio 0
	s_barrier
; #define PG8_STAGEA(bufoff, gbase, h) do { if constexpr (GATHER) { PG8_STAGE(bufoff, gbase, vA[h]); } else { PG8_STAGE(bufoff, (gbase) + (h) * hstepA, voffA); } } while (0)
; #define PG8_LDA(dst, b, h) do { _Pragma("unroll") for (int m = 0; m < 4; ++m) _Pragma("unroll") for (int k = 0; k < 2; ++k) dst[m][k] = *(const LAS bf16x8*)(lds + PG8_SA(b, h) + aoff + m * 2048 + k * 1024); } while (0)
; #define PG8_MM(ai, bj, At, Bt) do { if constexpr (Epi::F8MMA) PG8_MMA8(ai, bj, At, Bt##8); else PG8_MMA(ai, bj, At, Bt); } while (0)
; #define PG8_WAIT_V(n) asm volatile("s_waitcnt vmcnt(" #n ")" ::: "memory")
; #define PG8_WAIT_L(n) asm volatile("s_waitcnt lgkmcnt(" #n ")" ::: "memory")
; #define PG8_BAR __builtin_amdgcn_s_barrier()
; #define PG8_SCHED __builtin_amdgcn_sched_barrier(0)
; template <class Epi, class Sched>
; __device__ __forceinline__ void gemm_phase(const int tid, LAS unsigned char* lds, const char* Abase, const int lda, const int ldb, const int K, const Sched& S, const Epi& E) {
;     ...
;             PG8_LDB(B0, 0, 0); PG8_LDB(B1, 0, 1); PG8_SCHED; PG8_LDA(At, 0, 0); PG8_STAGEA(PG8_SA(1, 1), a1, 1);
;     ...
;             PG8_LDA(At, 0, 1); PG8_STAGE(PG8_SB(0, 0), b2, voffB); PG8_STAGE(PG8_SB(0, 1), b2 + hstepB, voffB); PG8_STAGEA(PG8_SA(0, 0), a2, 0);
;             PG8_WAIT_V(8); PG8_WAIT_L(0); PG8_BAR; PG8_MM(1, 0, At, B0); PG8_MM(1, 1, At, B1); PG8_BAR; PG8_SCHED;
;             PG8_LDB(B0, 1, 0); PG8_LDB(B1, 1, 1); PG8_SCHED; PG8_LDA(At, 1, 0); PG8_STAGEA(PG8_SA(0, 1), a2, 1);
;             PG8_WAIT_V(8); PG8_WAIT_L(0); PG8_BAR; PG8_MM(0, 0, At, B0); PG8_MM(0, 1, At, B1); PG8_BAR; PG8_SCHED;
;             PG8_LDA(At, 1, 1); PG8_STAGE(PG8_SB(1, 0), b3, voffB); PG8_STAGE(PG8_SB(1, 1), b3 + hstepB, voffB); PG8_STAGEA(PG8_SA(1, 0), a3, 0);
;             PG8_WAIT_V(8); PG8_WAIT_L(0); PG8_BAR; PG8_MM(1, 0, At, B0); PG8_MM(1, 1, At, B1); PG8_BAR; PG8_SCHED;
.Lmid_gu:
	s_add_i32 vcc_lo, 0, 0x18000
	s_add_i32 vcc_hi, 0, 0x1c000
	ds_read_b128 v[4:7], v234
	ds_read_b128 v[8:11], v234 offset:1024
	ds_read_b128 v[12:15], v234 offset:2048
	ds_read_b128 v[16:19], v234 offset:3072
	ds_read_b128 v[20:23], v235
	ds_read_b128 v[24:27], v235 offset:1024
	ds_read_b128 v[28:31], v235 offset:2048
	ds_read_b128 v[32:35], v235 offset:3072
	s_mov_b32 m0, s83
	ds_read_b128 v[36:39], v244 offset:32768
	ds_read_b128 v[40:43], v244 offset:33792
	ds_read_b128 v[44:47], v244 offset:34816
	ds_read_b128 v[48:51], v244 offset:35840
	ds_read_b128 v[52:55], v244 offset:36864
	ds_read_b128 v[56:59], v244 offset:37888
	ds_read_b128 v[60:63], v244 offset:38912
	ds_read_b128 v[64:67], v244 offset:39936
	v_lshl_add_u64 v[214:215], s[70:71], 0, v[214:215]
	global_load_lds_dwordx4 v[214:215], off
	v_lshl_add_u64 v[212:213], s[70:71], 0, v[212:213]
	s_mov_b32 m0, s86
	s_nop 0
	global_load_lds_dwordx4 v[212:213], off
	s_waitcnt vmcnt(8)
	s_waitcnt lgkmcnt(0)
	s_barrier
	s_setprio 1
	s_waitcnt lgkmcnt(0)
	v_mfma_scale_f32_16x16x128_f8f6f4 v[192:195], v[4:11], v[36:43], v[192:195], v220, v216 op_sel_hi:[0,0,0]
	v_mfma_scale_f32_16x16x128_f8f6f4 v[188:191], v[12:19], v[36:43], v[188:191], v220, v216 op_sel_hi:[0,0,0]
	v_mfma_scale_f32_16x16x128_f8f6f4 v[184:187], v[4:11], v[44:51], v[184:187], v220, v216 op_sel_hi:[0,0,0]
	v_mfma_scale_f32_16x16x128_f8f6f4 v[180:183], v[12:19], v[44:51], v[180:183], v220, v216 op_sel_hi:[0,0,0]
	v_mfma_scale_f32_16x16x128_f8f6f4 v[176:179], v[4:11], v[52:59], v[176:179], v220, v216 op_sel_hi:[0,0,0]
	v_mfma_scale_f32_16x16x128_f8f6f4 v[172:175], v[12:19], v[52:59], v[172:175], v220, v216 op_sel_hi:[0,0,0]
	v_mfma_scale_f32_16x16x128_f8f6f4 v[168:171], v[4:11], v[60:67], v[168:171], v220, v216 op_sel_hi:[0,0,0]
	v_mfma_scale_f32_16x16x128_f8f6f4 v[164:167], v[12:19], v[60:67], v[164:167], v220, v216 op_sel_hi:[0,0,0]
	s_setprio 0
	s_setprio 1
	v_mfma_scale_f32_16x16x128_f8f6f4 v[160:163], v[20:27], v[36:43], v[160:163], v216, v216 op_sel_hi:[0,0,0]
	v_mfma_scale_f32_16x16x128_f8f6f4 v[156:159], v[28:35], v[36:43], v[156:159], v216, v216 op_sel_hi:[0,0,0]
	v_mfma_scale_f32_16x16x128_f8f6f4 v[152:155], v[20:27], v[44:51], v[152:155], v216, v216 op_sel_hi:[0,0,0]
	v_mfma_scale_f32_16x16x128_f8f6f4 v[148:151], v[28:35], v[44:51], v[148:151], v216, v216 op_sel_hi:[0,0,0]
	v_mfma_scale_f32_16x16x128_f8f6f4 v[144:147], v[20:27], v[52:59], v[144:147], v216, v216 op_sel_hi:[0,0,0]
	v_mfma_scale_f32_16x16x128_f8f6f4 v[140:143], v[28:35], v[52:59], v[140:143], v216, v216 op_sel_hi:[0,0,0]
	v_mfma_scale_f32_16x16x128_f8f6f4 v[136:139], v[20:27], v[60:67], v[136:139], v216, v216 op_sel_hi:[0,0,0]
	v_mfma_scale_f32_16x16x128_f8f6f4 v[132:135], v[28:35], v[60:67], v[132:135], v216, v216 op_sel_hi:[0,0,0]
	s_setprio 0
	s_barrier
	s_add_i32 s70, vcc_lo, s72
	s_mov_b32 m0, s70
	ds_read_b128 v[36:39], v244 offset:49152
	ds_read_b128 v[40:43], v244 offset:50176
	ds_read_b128 v[44:47], v244 offset:51200
	ds_read_b128 v[48:51], v244 offset:52224
	ds_read_b128 v[52:55], v244 offset:53248
	ds_read_b128 v[56:59], v244 offset:54272
	ds_read_b128 v[60:63], v244 offset:55296
	ds_read_b128 v[64:67], v244 offset:56320
	v_lshl_add_u64 v[212:213], s[68:69], 0, v[198:199]
	global_load_lds_dwordx4 v[212:213], off
	s_add_i32 m0, s70, 0x2000
	s_add_u32 s66, s66, 0x20080
	v_lshl_add_u64 v[212:213], s[68:69], 0, v[200:201]
	s_addc_u32 s67, s67, 0
	s_add_i32 s68, vcc_hi, s72
	global_load_lds_dwordx4 v[212:213], off
	v_lshl_add_u64 v[212:213], s[66:67], 0, v[198:199]
	s_mov_b32 m0, s68
	s_nop 0
	global_load_lds_dwordx4 v[212:213], off
	v_lshl_add_u64 v[212:213], s[66:67], 0, v[200:201]
	s_add_i32 m0, s68, 0x2000
	s_nop 0
	global_load_lds_dwordx4 v[212:213], off
	s_mov_b32 m0, s89
	s_nop 0
	global_load_lds_dwordx4 v196, s[64:65]
	s_mov_b32 m0, s90
	s_nop 0
	global_load_lds_dwordx4 v0, s[64:65]
	s_waitcnt vmcnt(8)
	s_waitcnt lgkmcnt(0)
	s_barrier
	s_setprio 1
	s_waitcnt lgkmcnt(0)
	v_mfma_scale_f32_16x16x128_f8f6f4 v[128:131], v[4:11], v[36:43], v[128:131], v220, v216 op_sel_hi:[0,0,0]
	v_mfma_scale_f32_16x16x128_f8f6f4 v[124:127], v[12:19], v[36:43], v[124:127], v220, v216 op_sel_hi:[0,0,0]
	v_mfma_scale_f32_16x16x128_f8f6f4 v[120:123], v[4:11], v[44:51], v[120:123], v220, v216 op_sel_hi:[0,0,0]
	v_mfma_scale_f32_16x16x128_f8f6f4 v[116:119], v[12:19], v[44:51], v[116:119], v220, v216 op_sel_hi:[0,0,0]
	v_mfma_scale_f32_16x16x128_f8f6f4 v[112:115], v[4:11], v[52:59], v[112:115], v220, v216 op_sel_hi:[0,0,0]
	v_mfma_scale_f32_16x16x128_f8f6f4 v[108:111], v[12:19], v[52:59], v[108:111], v220, v216 op_sel_hi:[0,0,0]
	v_mfma_scale_f32_16x16x128_f8f6f4 v[104:107], v[4:11], v[60:67], v[104:107], v220, v216 op_sel_hi:[0,0,0]
	v_mfma_scale_f32_16x16x128_f8f6f4 v[100:103], v[12:19], v[60:67], v[100:103], v220, v216 op_sel_hi:[0,0,0]
	s_setprio 0
	s_setprio 1
	v_mfma_scale_f32_16x16x128_f8f6f4 v[96:99], v[20:27], v[36:43], v[96:99], v216, v216 op_sel_hi:[0,0,0]
	v_mfma_scale_f32_16x16x128_f8f6f4 v[92:95], v[28:35], v[36:43], v[92:95], v216, v216 op_sel_hi:[0,0,0]
	v_mfma_scale_f32_16x16x128_f8f6f4 v[88:91], v[20:27], v[44:51], v[88:91], v216, v216 op_sel_hi:[0,0,0]
	v_mfma_scale_f32_16x16x128_f8f6f4 v[84:87], v[28:35], v[44:51], v[84:87], v216, v216 op_sel_hi:[0,0,0]
	v_mfma_scale_f32_16x16x128_f8f6f4 v[80:83], v[20:27], v[52:59], v[80:83], v216, v216 op_sel_hi:[0,0,0]
	v_mfma_scale_f32_16x16x128_f8f6f4 v[76:79], v[28:35], v[52:59], v[76:79], v216, v216 op_sel_hi:[0,0,0]
	v_mfma_scale_f32_16x16x128_f8f6f4 v[72:75], v[20:27], v[60:67], v[72:75], v216, v216 op_sel_hi:[0,0,0]
	v_mfma_scale_f32_16x16x128_f8f6f4 v[68:71], v[28:35], v[60:67], v[68:71], v216, v216 op_sel_hi:[0,0,0]
	s_setprio 0
	s_barrier
	s_add_u32 s62, s62, 0x100
	s_addc_u32 s63, s63, 0
	s_cmp_ge_i32 s41, s25
	s_cbranch_scc1 .LBB0_1598
.LBB0_1596:
	ds_read_b128 v[20:23], v230
	ds_read_b128 v[24:27], v230 offset:1024
	ds_read_b128 v[28:31], v230 offset:2048
	ds_read_b128 v[32:35], v230 offset:3072
	ds_read_b128 v[4:7], v231
	ds_read_b128 v[8:11], v231 offset:1024
	ds_read_b128 v[12:15], v231 offset:2048
	ds_read_b128 v[16:19], v231 offset:3072
	s_cmp_eq_u32 s91, s41
	s_cselect_b64 s[66:67], -1, 0
	s_add_u32 s64, s46, s62
	s_addc_u32 s65, s47, s63
	s_add_u32 s64, s64, 0xffffff80
	s_addc_u32 s65, s65, -1
	s_add_i32 m0, s73, 0xc000
	s_add_i32 s68, s73, 0xe000
	s_cmp_lg_u32 s91, s41
	ds_read_b128 v[60:63], v244
	ds_read_b128 v[64:67], v244 offset:1024
	ds_read_b128 v[52:55], v244 offset:2048
	ds_read_b128 v[56:59], v244 offset:3072
	ds_read_b128 v[44:47], v244 offset:4096
	ds_read_b128 v[48:51], v244 offset:5120
	ds_read_b128 v[36:39], v244 offset:6144
	ds_read_b128 v[40:43], v244 offset:7168
	global_load_lds_dwordx4 v2, s[64:65]
	s_mov_b32 m0, s68
	s_nop 0
	global_load_lds_dwordx4 v202, s[64:65]
	s_cbranch_scc0 .LBB0_1594
	v_mov_b32_e32 v203, v3
	v_mov_b64_e32 v[212:213], v[202:203]
	v_mov_b64_e32 v[214:215], v[2:3]
	s_cmp_eq_u32 s41, 0
	s_cbranch_scc1 .Lpeel_gu
	s_branch .LBB0_1595

; #define PG8_STAGEA(bufoff, gbase, h) do { if constexpr (GATHER) { PG8_STAGE(bufoff, gbase, vA[h]); } else { PG8_STAGE(bufoff, (gbase) + (h) * hstepA, voffA); } } while (0)
; #define PG8_LDA(dst, b, h) do { _Pragma("unroll") for (int m = 0; m < 4; ++m) _Pragma("unroll") for (int k = 0; k < 2; ++k) dst[m][k] = *(const LAS bf16x8*)(lds + PG8_SA(b, h) + aoff + m * 2048 + k * 1024); } while (0)
; #define PG8_SCHED __builtin_amdgcn_sched_barrier(0)
; template <class Epi, class Sched>
; __device__ __forceinline__ void gemm_phase(const int tid, LAS unsigned char* lds, const char* Abase, const int lda, const int ldb, const int K, const Sched& S, const Epi& E) {
;     ...
; #pragma unroll 1
;         for (int t = 0; t < nt; t += 2) {
;             const bool last = (t == nt - 2);
;             const char* a1 = cA + (size_t)(t + 1) * kstepA;
;             const char* a2 = last ? nA : cA + (size_t)(t + 2) * kstepA; const char* b2 = last ? nB : cB + (size_t)(t + 2) * kstep;
;             const char* a3 = a2 + kstepA; const char* b3 = b2 + kstep;
;             PG8_LDB(B0, 0, 0); PG8_LDB(B1, 0, 1); PG8_SCHED; PG8_LDA(At, 0, 0); PG8_STAGEA(PG8_SA(1, 1), a1, 1);
.LBB0_1705:
	s_andn2_b64 vcc, exec, s[46:47]
	s_cbranch_vccnz .LBB0_1716
	s_add_u32 s87, s56, 0x100
	v_mov_b32_e32 v209, v3
	v_mov_b32_e32 v207, v3
	s_addc_u32 s88, s57, 0
	s_mov_b32 s89, 0
	s_mov_b64 s[56:57], 0x10000
	v_add_u32_e32 v230, 0x10000, v199
	v_add_u32_e32 v231, 0x14000, v199
	v_add_u32_e32 v234, 0x18000, v199
	v_add_u32_e32 v235, 0x1c000, v199
	s_branch .LBB0_1709

; #define PG8_STAGEA(bufoff, gbase, h) do { if constexpr (GATHER) { PG8_STAGE(bufoff, gbase, vA[h]); } else { PG8_STAGE(bufoff, (gbase) + (h) * hstepA, voffA); } } while (0)
; #define PG8_LDA(dst, b, h) do { _Pragma("unroll") for (int m = 0; m < 4; ++m) _Pragma("unroll") for (int k = 0; k < 2; ++k) dst[m][k] = *(const LAS bf16x8*)(lds + PG8_SA(b, h) + aoff + m * 2048 + k * 1024); } while (0)
; #define PG8_MM(ai, bj, At, Bt) do { if constexpr (Epi::F8MMA) PG8_MMA8(ai, bj, At, Bt##8); else PG8_MMA(ai, bj, At, Bt); } while (0)
; #define PG8_WAIT_V(n) asm volatile("s_waitcnt vmcnt(" #n ")" ::: "memory")
; #define PG8_WAIT_L(n) asm volatile("s_waitcnt lgkmcnt(" #n ")" ::: "memory")
; #define PG8_BAR __builtin_amdgcn_s_barrier()
; #define PG8_SCHED __builtin_amdgcn_sched_barrier(0)
; template <class Epi, class Sched>
; __device__ __forceinline__ void gemm_phase(const int tid, LAS unsigned char* lds, const char* Abase, const int lda, const int ldb, const int K, const Sched& S, const Epi& E) {
;     ...
;             PG8_LDB(B0, 0, 0); PG8_LDB(B1, 0, 1); PG8_SCHED; PG8_LDA(At, 0, 0); PG8_STAGEA(PG8_SA(1, 1), a1, 1);
;             if constexpr (GATHER) { if (last) {
; #pragma unroll
;                 for (int h = 0; h < 2; ++h)
; #pragma unroll
;                     for (int i = 0; i < 2; ++i) vA[h][i] = vAn[h][i]; } }
;             PG8_WAIT_V(8); PG8_WAIT_L(0); PG8_BAR; PG8_MM(0, 0, At, B0); PG8_MM(0, 1, At, B1); PG8_BAR; PG8_SCHED;
;             PG8_LDA(At, 0, 1); PG8_STAGE(PG8_SB(0, 0), b2, voffB); PG8_STAGE(PG8_SB(0, 1), b2 + hstepB, voffB); PG8_STAGEA(PG8_SA(0, 0), a2, 0);
;             PG8_WAIT_V(8); PG8_WAIT_L(0); PG8_BAR; PG8_MM(1, 0, At, B0); PG8_MM(1, 1, At, B1); PG8_BAR; PG8_SCHED;
;             PG8_LDB(B0, 1, 0); PG8_LDB(B1, 1, 1); PG8_SCHED; PG8_LDA(At, 1, 0); PG8_STAGEA(PG8_SA(0, 1), a2, 1);
;             PG8_WAIT_V(8); PG8_WAIT_L(0); PG8_BAR; PG8_MM(0, 0, At, B0); PG8_MM(0, 1, At, B1); PG8_BAR; PG8_SCHED;
.LBB0_1708:
	s_add_i32 s89, s89, 2
	s_and_b64 s[60:61], s[62:63], exec
	s_cselect_b32 s61, 0, s56
	s_cselect_b32 s60, 0, s57
	s_add_u32 s66, s2, s61
	s_addc_u32 s67, s3, s60
	s_add_u32 s60, s66, 0x8000
	s_addc_u32 s61, s67, 0
	s_waitcnt vmcnt(8)
	s_and_b64 s[62:63], s[62:63], exec
	s_waitcnt lgkmcnt(0)
	s_cselect_b32 s62, s54, s87
	s_cselect_b32 s63, s55, s88
	s_add_u32 s64, s62, 0x80
	s_addc_u32 s65, s63, 0
	s_barrier
	s_setprio 1
	s_waitcnt lgkmcnt(0)
	v_mfma_scale_f32_16x16x128_f8f6f4 v[192:195], v[20:27], v[60:67], 0, v224, v216 op_sel_hi:[0,0,0]
	v_mfma_scale_f32_16x16x128_f8f6f4 v[188:191], v[28:35], v[60:67], 0, v224, v216 op_sel_hi:[0,0,0]
	v_mfma_scale_f32_16x16x128_f8f6f4 v[176:179], v[20:27], v[52:59], 0, v224, v216 op_sel_hi:[0,0,0]
	v_mfma_scale_f32_16x16x128_f8f6f4 v[172:175], v[28:35], v[52:59], 0, v224, v216 op_sel_hi:[0,0,0]
	v_mfma_scale_f32_16x16x128_f8f6f4 v[160:163], v[20:27], v[44:51], 0, v224, v216 op_sel_hi:[0,0,0]
	v_mfma_scale_f32_16x16x128_f8f6f4 v[156:159], v[28:35], v[44:51], 0, v224, v216 op_sel_hi:[0,0,0]
	v_mfma_scale_f32_16x16x128_f8f6f4 v[144:147], v[20:27], v[36:43], 0, v224, v216 op_sel_hi:[0,0,0]
	v_mfma_scale_f32_16x16x128_f8f6f4 v[140:143], v[28:35], v[36:43], 0, v224, v216 op_sel_hi:[0,0,0]
	s_setprio 0
	s_setprio 1
	v_mfma_scale_f32_16x16x128_f8f6f4 v[184:187], v[4:11], v[60:67], 0, v224, v216 op_sel_hi:[0,0,0]
	v_mfma_scale_f32_16x16x128_f8f6f4 v[180:183], v[12:19], v[60:67], 0, v224, v216 op_sel_hi:[0,0,0]
	v_mfma_scale_f32_16x16x128_f8f6f4 v[168:171], v[4:11], v[52:59], 0, v224, v216 op_sel_hi:[0,0,0]
	v_mfma_scale_f32_16x16x128_f8f6f4 v[164:167], v[12:19], v[52:59], 0, v224, v216 op_sel_hi:[0,0,0]
	v_mfma_scale_f32_16x16x128_f8f6f4 v[152:155], v[4:11], v[44:51], 0, v224, v216 op_sel_hi:[0,0,0]
	v_mfma_scale_f32_16x16x128_f8f6f4 v[148:151], v[12:19], v[44:51], 0, v224, v216 op_sel_hi:[0,0,0]
	v_mfma_scale_f32_16x16x128_f8f6f4 v[136:139], v[4:11], v[36:43], 0, v224, v216 op_sel_hi:[0,0,0]
	v_mfma_scale_f32_16x16x128_f8f6f4 v[132:135], v[12:19], v[36:43], 0, v224, v216 op_sel_hi:[0,0,0]
	s_setprio 0
	s_barrier
	s_mov_b32 m0, s28
	s_add_u32 s90, s62, 0x2000
	ds_read_b128 v[36:39], v243 offset:16384
	ds_read_b128 v[40:43], v243 offset:17408
	ds_read_b128 v[44:47], v243 offset:18432
	ds_read_b128 v[48:51], v243 offset:19456
	ds_read_b128 v[52:55], v243 offset:20480
	ds_read_b128 v[56:59], v243 offset:21504
	ds_read_b128 v[60:63], v243 offset:22528
	ds_read_b128 v[64:67], v243 offset:23552
	v_lshl_add_u64 v[228:229], s[62:63], 0, v[0:1]
	global_load_lds_dwordx4 v[228:229], off
	v_lshl_add_u64 v[228:229], s[62:63], 0, v[196:197]
	s_mov_b32 m0, s29
	s_addc_u32 s91, s63, 0
	global_load_lds_dwordx4 v[228:229], off
	v_lshl_add_u64 v[228:229], s[90:91], 0, v[0:1]
	s_mov_b32 m0, s68
	s_nop 0
	global_load_lds_dwordx4 v[228:229], off
	v_lshl_add_u64 v[228:229], s[90:91], 0, v[196:197]
	s_mov_b32 m0, s69
	s_nop 0
	global_load_lds_dwordx4 v[228:229], off
	s_mov_b32 m0, s25
	s_nop 0
	global_load_lds_dwordx4 v200, s[66:67]
	s_mov_b32 m0, s70
	s_nop 0
	global_load_lds_dwordx4 v198, s[66:67]
	s_waitcnt vmcnt(8)
	s_waitcnt lgkmcnt(0)
	s_barrier
	s_setprio 1
	s_waitcnt lgkmcnt(0)
	v_mfma_scale_f32_16x16x128_f8f6f4 v[128:131], v[20:27], v[36:43], 0, v224, v216 op_sel_hi:[0,0,0]
	v_mfma_scale_f32_16x16x128_f8f6f4 v[124:127], v[28:35], v[36:43], 0, v224, v216 op_sel_hi:[0,0,0]
	v_mfma_scale_f32_16x16x128_f8f6f4 v[112:115], v[20:27], v[44:51], 0, v224, v216 op_sel_hi:[0,0,0]
	v_mfma_scale_f32_16x16x128_f8f6f4 v[108:111], v[28:35], v[44:51], 0, v224, v216 op_sel_hi:[0,0,0]
	v_mfma_scale_f32_16x16x128_f8f6f4 v[96:99], v[20:27], v[52:59], 0, v224, v216 op_sel_hi:[0,0,0]
	v_mfma_scale_f32_16x16x128_f8f6f4 v[92:95], v[28:35], v[52:59], 0, v224, v216 op_sel_hi:[0,0,0]
	v_mfma_scale_f32_16x16x128_f8f6f4 v[80:83], v[20:27], v[60:67], 0, v224, v216 op_sel_hi:[0,0,0]
	v_mfma_scale_f32_16x16x128_f8f6f4 v[76:79], v[28:35], v[60:67], 0, v224, v216 op_sel_hi:[0,0,0]
	s_setprio 0
	s_setprio 1
	v_mfma_scale_f32_16x16x128_f8f6f4 v[120:123], v[4:11], v[36:43], 0, v224, v216 op_sel_hi:[0,0,0]
	v_mfma_scale_f32_16x16x128_f8f6f4 v[116:119], v[12:19], v[36:43], 0, v224, v216 op_sel_hi:[0,0,0]
	v_mfma_scale_f32_16x16x128_f8f6f4 v[104:107], v[4:11], v[44:51], 0, v224, v216 op_sel_hi:[0,0,0]
	v_mfma_scale_f32_16x16x128_f8f6f4 v[100:103], v[12:19], v[44:51], 0, v224, v216 op_sel_hi:[0,0,0]
	v_mfma_scale_f32_16x16x128_f8f6f4 v[88:91], v[4:11], v[52:59], 0, v224, v216 op_sel_hi:[0,0,0]
	v_mfma_scale_f32_16x16x128_f8f6f4 v[84:87], v[12:19], v[52:59], 0, v224, v216 op_sel_hi:[0,0,0]
	v_mfma_scale_f32_16x16x128_f8f6f4 v[72:75], v[4:11], v[60:67], 0, v224, v216 op_sel_hi:[0,0,0]
	v_mfma_scale_f32_16x16x128_f8f6f4 v[68:71], v[12:19], v[60:67], 0, v224, v216 op_sel_hi:[0,0,0]
	s_setprio 0
	s_barrier
	s_add_i32 s90, 0, 0x18000
	s_add_i32 s91, 0, 0x1c000
	ds_read_b128 v[4:7], v234
	ds_read_b128 v[8:11], v234 offset:1024
	ds_read_b128 v[12:15], v234 offset:2048
	ds_read_b128 v[16:19], v234 offset:3072
	ds_read_b128 v[20:23], v235
	ds_read_b128 v[24:27], v235 offset:1024
	ds_read_b128 v[28:31], v235 offset:2048
	ds_read_b128 v[32:35], v235 offset:3072
	s_mov_b32 m0, s71
	ds_read_b128 v[36:39], v243 offset:32768
	ds_read_b128 v[40:43], v243 offset:33792
	ds_read_b128 v[44:47], v243 offset:34816
	ds_read_b128 v[48:51], v243 offset:35840
	ds_read_b128 v[52:55], v243 offset:36864
	ds_read_b128 v[56:59], v243 offset:37888
	ds_read_b128 v[60:63], v243 offset:38912
	ds_read_b128 v[64:67], v243 offset:39936
	v_lshl_add_u64 v[212:213], s[66:67], 0, v[212:213]
	global_load_lds_dwordx4 v[212:213], off
	v_lshl_add_u64 v[210:211], s[66:67], 0, v[210:211]
	s_mov_b32 m0, s72
	s_nop 0
	global_load_lds_dwordx4 v[210:211], off
	s_waitcnt vmcnt(8)
	s_waitcnt lgkmcnt(0)
	s_barrier
; #define PG8_STAGEA(bufoff, gbase, h) do { if constexpr (GATHER) { PG8_STAGE(bufoff, gbase, vA[h]); } else { PG8_STAGE(bufoff, (gbase) + (h) * hstepA, voffA); } } while (0)
; #define PG8_LDA(dst, b, h) do { _Pragma("unroll") for (int m = 0; m < 4; ++m) _Pragma("unroll") for (int k = 0; k < 2; ++k) dst[m][k] = *(const LAS bf16x8*)(lds + PG8_SA(b, h) + aoff + m * 2048 + k * 1024); } while (0)
; #define PG8_MM(ai, bj, At, Bt) do { if constexpr (Epi::F8MMA) PG8_MMA8(ai, bj, At, Bt##8); else PG8_MMA(ai, bj, At, Bt); } while (0)
; #define PG8_WAIT_V(n) asm volatile("s_waitcnt vmcnt(" #n ")" ::: "memory")
; #define PG8_WAIT_L(n) asm volatile("s_waitcnt lgkmcnt(" #n ")" ::: "memory")
; #define PG8_BAR __builtin_amdgcn_s_barrier()
; #define PG8_SCHED __builtin_amdgcn_sched_barrier(0)
; template <class Epi, class Sched>
; __device__ __forceinline__ void gemm_phase(const int tid, LAS unsigned char* lds, const char* Abase, const int lda, const int ldb, const int K, const Sched& S, const Epi& E) {
;     ...
;             PG8_LDB(B0, 0, 0); PG8_LDB(B1, 0, 1); PG8_SCHED; PG8_LDA(At, 0, 0); PG8_STAGEA(PG8_SA(1, 1), a1, 1);
;     ...
;             PG8_WAIT_V(8); PG8_WAIT_L(0); PG8_BAR; PG8_MM(0, 0, At, B0); PG8_MM(0, 1, At, B1); PG8_BAR; PG8_SCHED;
;             PG8_LDA(At, 1, 1); PG8_STAGE(PG8_SB(1, 0), b3, voffB); PG8_STAGE(PG8_SB(1, 1), b3 + hstepB, voffB); PG8_STAGEA(PG8_SA(1, 0), a3, 0);
;             PG8_WAIT_V(8); PG8_WAIT_L(0); PG8_BAR; PG8_MM(1, 0, At, B0); PG8_MM(1, 1, At, B1); PG8_BAR; PG8_SCHED;
	s_setprio 1
	s_waitcnt lgkmcnt(0)
	v_mfma_scale_f32_16x16x128_f8f6f4 v[192:195], v[4:11], v[36:43], v[192:195], v224, v216 op_sel_hi:[0,0,0]
	v_mfma_scale_f32_16x16x128_f8f6f4 v[188:191], v[12:19], v[36:43], v[188:191], v224, v216 op_sel_hi:[0,0,0]
	v_mfma_scale_f32_16x16x128_f8f6f4 v[176:179], v[4:11], v[44:51], v[176:179], v224, v216 op_sel_hi:[0,0,0]
	v_mfma_scale_f32_16x16x128_f8f6f4 v[172:175], v[12:19], v[44:51], v[172:175], v224, v216 op_sel_hi:[0,0,0]
	v_mfma_scale_f32_16x16x128_f8f6f4 v[160:163], v[4:11], v[52:59], v[160:163], v224, v216 op_sel_hi:[0,0,0]
	v_mfma_scale_f32_16x16x128_f8f6f4 v[156:159], v[12:19], v[52:59], v[156:159], v224, v216 op_sel_hi:[0,0,0]
	v_mfma_scale_f32_16x16x128_f8f6f4 v[144:147], v[4:11], v[60:67], v[144:147], v224, v216 op_sel_hi:[0,0,0]
	v_mfma_scale_f32_16x16x128_f8f6f4 v[140:143], v[12:19], v[60:67], v[140:143], v224, v216 op_sel_hi:[0,0,0]
	s_setprio 0
	s_setprio 1
	v_mfma_scale_f32_16x16x128_f8f6f4 v[184:187], v[20:27], v[36:43], v[184:187], v224, v216 op_sel_hi:[0,0,0]
	v_mfma_scale_f32_16x16x128_f8f6f4 v[180:183], v[28:35], v[36:43], v[180:183], v224, v216 op_sel_hi:[0,0,0]
	v_mfma_scale_f32_16x16x128_f8f6f4 v[168:171], v[20:27], v[44:51], v[168:171], v224, v216 op_sel_hi:[0,0,0]
	v_mfma_scale_f32_16x16x128_f8f6f4 v[164:167], v[28:35], v[44:51], v[164:167], v224, v216 op_sel_hi:[0,0,0]
	v_mfma_scale_f32_16x16x128_f8f6f4 v[152:155], v[20:27], v[52:59], v[152:155], v224, v216 op_sel_hi:[0,0,0]
	v_mfma_scale_f32_16x16x128_f8f6f4 v[148:151], v[28:35], v[52:59], v[148:151], v224, v216 op_sel_hi:[0,0,0]
	v_mfma_scale_f32_16x16x128_f8f6f4 v[136:139], v[20:27], v[60:67], v[136:139], v224, v216 op_sel_hi:[0,0,0]
	v_mfma_scale_f32_16x16x128_f8f6f4 v[132:135], v[28:35], v[60:67], v[132:135], v224, v216 op_sel_hi:[0,0,0]
	s_setprio 0
	s_barrier
	s_add_i32 s66, s90, s22
	s_mov_b32 m0, s66
	ds_read_b128 v[36:39], v243 offset:49152
	ds_read_b128 v[40:43], v243 offset:50176
	ds_read_b128 v[44:47], v243 offset:51200
	ds_read_b128 v[48:51], v243 offset:52224
	ds_read_b128 v[52:55], v243 offset:53248
	ds_read_b128 v[56:59], v243 offset:54272
	ds_read_b128 v[60:63], v243 offset:55296
	ds_read_b128 v[64:67], v243 offset:56320
	v_lshl_add_u64 v[210:211], s[64:65], 0, v[0:1]
	global_load_lds_dwordx4 v[210:211], off
	s_add_i32 m0, s66, 0x2000
	s_add_u32 s62, s62, 0x2080
	v_lshl_add_u64 v[210:211], s[64:65], 0, v[196:197]
	s_addc_u32 s63, s63, 0
	s_add_i32 s64, s91, s22
	global_load_lds_dwordx4 v[210:211], off
	v_lshl_add_u64 v[210:211], s[62:63], 0, v[0:1]
	s_mov_b32 m0, s64
	s_nop 0
	global_load_lds_dwordx4 v[210:211], off
	v_lshl_add_u64 v[210:211], s[62:63], 0, v[196:197]
	s_add_i32 m0, s64, 0x2000
	s_nop 0
	global_load_lds_dwordx4 v[210:211], off
	s_mov_b32 m0, s73
	s_nop 0
	global_load_lds_dwordx4 v200, s[60:61]
	s_mov_b32 m0, s76
	s_nop 0
	global_load_lds_dwordx4 v198, s[60:61]
	s_waitcnt vmcnt(8)
	s_waitcnt lgkmcnt(0)
	s_barrier
	s_setprio 1
	s_waitcnt lgkmcnt(0)
	v_mfma_scale_f32_16x16x128_f8f6f4 v[128:131], v[4:11], v[36:43], v[128:131], v224, v216 op_sel_hi:[0,0,0]
	v_mfma_scale_f32_16x16x128_f8f6f4 v[124:127], v[12:19], v[36:43], v[124:127], v224, v216 op_sel_hi:[0,0,0]
	v_mfma_scale_f32_16x16x128_f8f6f4 v[112:115], v[4:11], v[44:51], v[112:115], v224, v216 op_sel_hi:[0,0,0]
	v_mfma_scale_f32_16x16x128_f8f6f4 v[108:111], v[12:19], v[44:51], v[108:111], v224, v216 op_sel_hi:[0,0,0]
	v_mfma_scale_f32_16x16x128_f8f6f4 v[96:99], v[4:11], v[52:59], v[96:99], v224, v216 op_sel_hi:[0,0,0]
	v_mfma_scale_f32_16x16x128_f8f6f4 v[92:95], v[12:19], v[52:59], v[92:95], v224, v216 op_sel_hi:[0,0,0]
	v_mfma_scale_f32_16x16x128_f8f6f4 v[80:83], v[4:11], v[60:67], v[80:83], v224, v216 op_sel_hi:[0,0,0]
	v_mfma_scale_f32_16x16x128_f8f6f4 v[76:79], v[12:19], v[60:67], v[76:79], v224, v216 op_sel_hi:[0,0,0]
	s_setprio 0
	s_setprio 1
	v_mfma_scale_f32_16x16x128_f8f6f4 v[120:123], v[20:27], v[36:43], v[120:123], v224, v216 op_sel_hi:[0,0,0]
	v_mfma_scale_f32_16x16x128_f8f6f4 v[116:119], v[28:35], v[36:43], v[116:119], v224, v216 op_sel_hi:[0,0,0]
	v_mfma_scale_f32_16x16x128_f8f6f4 v[104:107], v[20:27], v[44:51], v[104:107], v224, v216 op_sel_hi:[0,0,0]
	v_mfma_scale_f32_16x16x128_f8f6f4 v[100:103], v[28:35], v[44:51], v[100:103], v224, v216 op_sel_hi:[0,0,0]
	v_mfma_scale_f32_16x16x128_f8f6f4 v[88:91], v[20:27], v[52:59], v[88:91], v224, v216 op_sel_hi:[0,0,0]
	v_mfma_scale_f32_16x16x128_f8f6f4 v[84:87], v[28:35], v[52:59], v[84:87], v224, v216 op_sel_hi:[0,0,0]
	v_mfma_scale_f32_16x16x128_f8f6f4 v[72:75], v[20:27], v[60:67], v[72:75], v224, v216 op_sel_hi:[0,0,0]
	v_mfma_scale_f32_16x16x128_f8f6f4 v[68:71], v[28:35], v[60:67], v[68:71], v224, v216 op_sel_hi:[0,0,0]
	s_setprio 0
	s_barrier
	s_add_u32 s87, s87, 0x100
	s_addc_u32 s88, s88, 0
	s_add_u32 s56, s56, 0x10000
	s_addc_u32 s57, s57, 0
	s_cmp_ge_i32 s89, s5
	s_cbranch_scc1 .LBB0_1711
.LBB0_1709:
	ds_read_b128 v[20:23], v230
	ds_read_b128 v[24:27], v230 offset:1024
	ds_read_b128 v[28:31], v230 offset:2048
	ds_read_b128 v[32:35], v230 offset:3072
	ds_read_b128 v[4:7], v231
	ds_read_b128 v[8:11], v231 offset:1024
	ds_read_b128 v[12:15], v231 offset:2048
	ds_read_b128 v[16:19], v231 offset:3072
	s_cmp_eq_u32 s78, s89
	s_cselect_b64 s[62:63], -1, 0
	s_add_u32 s60, s2, s56
	s_addc_u32 s61, s3, s57
	s_add_u32 s60, s60, 0xffff8000
	s_addc_u32 s61, s61, -1
	s_add_i32 m0, s25, 0xc000
	s_add_i32 s64, s25, 0xe000
	s_cmp_lg_u32 s78, s89
	ds_read_b128 v[60:63], v243
	ds_read_b128 v[64:67], v243 offset:1024
	ds_read_b128 v[52:55], v243 offset:2048
	ds_read_b128 v[56:59], v243 offset:3072
	ds_read_b128 v[44:47], v243 offset:4096
	ds_read_b128 v[48:51], v243 offset:5120
	ds_read_b128 v[36:39], v243 offset:6144
	ds_read_b128 v[40:43], v243 offset:7168
	global_load_lds_dwordx4 v2, s[60:61]
	s_mov_b32 m0, s64
	s_nop 0
	global_load_lds_dwordx4 v202, s[60:61]
	s_cbranch_scc0 .LBB0_1707
	v_mov_b32_e32 v203, v3
	v_mov_b64_e32 v[210:211], v[202:203]
	v_mov_b64_e32 v[212:213], v[2:3]
	s_branch .LBB0_1708
